# v14 + nt on the P10 (act) and P11 (expert outputs Y) GEMM epilogue stores
# baseline (speedup 1.0000x reference)
.LBB0_1677:
	v_mov_b32_e32 v2, v238
	s_add_u32 s0, s79, 0xffffff00
	s_nop 15
	s_nop 15
	s_nop 15
	s_addc_u32 s1, s80, -1
	v_lshlrev_b32_e32 v3, 5, v2
	v_ashrrev_i32_e32 v4, 1, v2
	v_and_b32_e32 v3, 0x1e0, v3
	v_and_b32_e32 v5, -8, v4
	s_add_i32 s2, s33, s69
	v_add3_u32 v8, s53, v3, v5
	v_add_u32_e32 v10, s2, v4
	v_pk_mul_f32 v[4:5], v[190:191], s[28:29] op_sel_hi:[1,0]
	v_lshlrev_b32_e32 v2, 4, v2
	v_mul_f32_e32 v6, 0xbfb8aa3b, v4
	v_exp_f32_e32 v16, v6
	v_mul_f32_e32 v27, 0xbfb8aa3b, v5
	v_exp_f32_e32 v27, v27
	v_add_u32_e32 v9, s53, v2
	v_add_f32_e32 v22, 1.0, v16
	v_and_b32_e32 v11, 16, v2
	v_pk_mul_f32 v[2:3], v[192:193], s[28:29] op_sel_hi:[1,0]
	v_pk_mul_f32 v[16:17], v[158:159], s[30:31] op_sel_hi:[1,0]
	v_add_f32_e32 v25, 1.0, v27
	v_rcp_f32_e32 v23, v22
	s_nop 0
	v_mul_f32_e32 v4, v4, v23
	v_mul_f32_e32 v23, 0xbfb8aa3b, v2
	v_exp_f32_e32 v23, v23
	v_mul_f32_e32 v4, v4, v16
	v_add_f32_e32 v23, 1.0, v23
	v_mul_f32_e32 v22, 0xbfb8aa3b, v3
	v_rcp_f32_e32 v16, v25
	s_nop 0
	v_mul_f32_e32 v5, v5, v16
	v_exp_f32_e32 v22, v22
	v_mul_f32_e32 v5, v5, v17
	v_add_f32_e32 v22, 1.0, v22
	v_pk_mul_f32 v[14:15], v[160:161], s[30:31] op_sel_hi:[1,0]
	v_rcp_f32_e32 v16, v23
	s_nop 0
	v_mul_f32_e32 v2, v2, v16
	v_mul_f32_e32 v14, v2, v14
	v_pk_mul_f32 v[12:13], v[186:187], s[28:29] op_sel_hi:[1,0]
	v_rcp_f32_e32 v2, v22
	s_nop 0
	v_mul_f32_e32 v2, v3, v2
	v_mul_f32_e32 v3, v2, v15
	v_mul_f32_e32 v2, 0xbfb8aa3b, v12
	v_exp_f32_e32 v15, v2
	v_med3_f32 v4, v4, s75, v239
	v_med3_f32 v5, v5, s75, v239
	v_mov_b32_e32 v2, v203
	v_cvt_pk_fp8_f32 v2, v4, v5
	v_add_f32_e32 v4, 1.0, v15
	v_med3_f32 v14, v14, s75, v239
	v_med3_f32 v3, v3, s75, v239
	v_cvt_pk_fp8_f32 v2, v14, v3 op_sel:[0,0,1]
	v_mul_f32_e32 v16, 0xbfb8aa3b, v13
	v_exp_f32_e32 v16, v16
	s_nop 0
	v_add_f32_e32 v5, 1.0, v16
	v_pk_mul_f32 v[6:7], v[188:189], s[28:29] op_sel_hi:[1,0]
	v_mul_f32_e32 v14, 0xbfb8aa3b, v6
	v_exp_f32_e32 v14, v14
	v_rcp_f32_e32 v3, v4
	s_nop 0
	v_mul_f32_e32 v3, v12, v3
	v_add_f32_e32 v14, 1.0, v14
	v_rcp_f32_e32 v4, v5
	s_nop 0
	v_mul_f32_e32 v4, v13, v4
	v_mul_f32_e32 v13, 0xbfb8aa3b, v7
	v_exp_f32_e32 v13, v13
	s_nop 0
	v_add_f32_e32 v13, 1.0, v13
	v_rcp_f32_e32 v5, v14
	s_nop 0
	v_mul_f32_e32 v5, v6, v5
	v_pk_mul_f32 v[20:21], v[154:155], s[30:31] op_sel_hi:[1,0]
	v_mul_f32_e32 v3, v3, v20
	v_mul_f32_e32 v4, v4, v21
	v_pk_mul_f32 v[18:19], v[156:157], s[30:31] op_sel_hi:[1,0]
	v_rcp_f32_e32 v6, v13
	s_nop 0
	v_mul_f32_e32 v6, v7, v6
	v_med3_f32 v7, v3, s75, v239
	v_med3_f32 v4, v4, s75, v239
	v_mov_b32_e32 v3, v203
	v_cvt_pk_fp8_f32 v3, v7, v4
	v_mul_f32_e32 v4, v6, v19
	v_pk_mul_f32 v[6:7], v[182:183], s[28:29] op_sel_hi:[1,0]
	v_mul_f32_e32 v5, v5, v18
	v_mul_f32_e32 v12, 0xbfb8aa3b, v6
	v_exp_f32_e32 v18, v12
	v_mul_f32_e32 v29, 0xbfb8aa3b, v7
	v_exp_f32_e32 v29, v29
	v_med3_f32 v5, v5, s75, v239
	v_add_f32_e32 v24, 1.0, v18
	v_med3_f32 v4, v4, s75, v239
	v_cvt_pk_fp8_f32 v3, v5, v4 op_sel:[0,0,1]
	v_pk_mul_f32 v[4:5], v[184:185], s[28:29] op_sel_hi:[1,0]
	v_add_f32_e32 v27, 1.0, v29
	v_rcp_f32_e32 v25, v24
	s_nop 0
	v_mul_f32_e32 v6, v6, v25
	v_mul_f32_e32 v25, 0xbfb8aa3b, v4
	v_pk_mul_f32 v[18:19], v[150:151], s[30:31] op_sel_hi:[1,0]
	v_exp_f32_e32 v25, v25
	v_mul_f32_e32 v6, v6, v18
	v_add_f32_e32 v25, 1.0, v25
	v_mul_f32_e32 v24, 0xbfb8aa3b, v5
	v_rcp_f32_e32 v18, v27
	s_nop 0
	v_mul_f32_e32 v7, v7, v18
	v_exp_f32_e32 v24, v24
	v_mul_f32_e32 v7, v7, v19
	v_add_f32_e32 v24, 1.0, v24
	v_pk_mul_f32 v[16:17], v[152:153], s[30:31] op_sel_hi:[1,0]
	v_rcp_f32_e32 v18, v25
	s_nop 0
	v_mul_f32_e32 v4, v4, v18
	v_mul_f32_e32 v16, v4, v16
	v_pk_mul_f32 v[14:15], v[178:179], s[28:29] op_sel_hi:[1,0]
	v_rcp_f32_e32 v4, v24
	s_nop 0
	v_mul_f32_e32 v4, v5, v4
	v_mul_f32_e32 v5, v4, v17
	v_mul_f32_e32 v4, 0xbfb8aa3b, v14
	v_exp_f32_e32 v17, v4
	v_med3_f32 v6, v6, s75, v239
	v_med3_f32 v7, v7, s75, v239
	v_mov_b32_e32 v4, v203
	v_cvt_pk_fp8_f32 v4, v6, v7
	v_add_f32_e32 v6, 1.0, v17
	v_med3_f32 v16, v16, s75, v239
	v_med3_f32 v5, v5, s75, v239
	v_cvt_pk_fp8_f32 v4, v16, v5 op_sel:[0,0,1]
	v_mul_f32_e32 v18, 0xbfb8aa3b, v15
	v_exp_f32_e32 v18, v18
	s_nop 0
	v_add_f32_e32 v7, 1.0, v18
	v_pk_mul_f32 v[12:13], v[180:181], s[28:29] op_sel_hi:[1,0]
	v_mul_f32_e32 v16, 0xbfb8aa3b, v12
	v_exp_f32_e32 v16, v16
	v_rcp_f32_e32 v5, v6
	s_nop 0
	v_mul_f32_e32 v5, v14, v5
	v_add_f32_e32 v16, 1.0, v16
	v_rcp_f32_e32 v6, v7
	s_nop 0
	v_mul_f32_e32 v6, v15, v6
	v_mul_f32_e32 v15, 0xbfb8aa3b, v13
	v_exp_f32_e32 v15, v15
	s_nop 0
	v_add_f32_e32 v15, 1.0, v15
	v_rcp_f32_e32 v7, v16
	s_nop 0
	v_mul_f32_e32 v7, v12, v7
	v_pk_mul_f32 v[22:23], v[146:147], s[30:31] op_sel_hi:[1,0]
	v_mul_f32_e32 v5, v5, v22
	v_mul_f32_e32 v6, v6, v23
	v_pk_mul_f32 v[20:21], v[148:149], s[30:31] op_sel_hi:[1,0]
	v_rcp_f32_e32 v12, v15
	s_nop 0
	v_mul_f32_e32 v12, v13, v12
	v_med3_f32 v13, v5, s75, v239
	v_med3_f32 v6, v6, s75, v239
	v_mov_b32_e32 v5, v203
	v_cvt_pk_fp8_f32 v5, v13, v6
	v_mul_f32_e32 v6, v12, v21
	v_pk_mul_f32 v[12:13], v[174:175], s[28:29] op_sel_hi:[1,0]
	v_mul_f32_e32 v7, v7, v20
	v_mul_f32_e32 v14, 0xbfb8aa3b, v12
	v_exp_f32_e32 v20, v14
	v_mul_f32_e32 v31, 0xbfb8aa3b, v13
	v_exp_f32_e32 v31, v31
	v_med3_f32 v7, v7, s75, v239
	v_add_f32_e32 v26, 1.0, v20
	v_med3_f32 v6, v6, s75, v239
	v_cvt_pk_fp8_f32 v5, v7, v6 op_sel:[0,0,1]
	v_lshl_or_b32 v6, s18, 7, v11
	v_add_f32_e32 v29, 1.0, v31
	v_or_b32_e32 v11, s70, v6
	v_pk_mul_f32 v[6:7], v[176:177], s[28:29] op_sel_hi:[1,0]
	v_rcp_f32_e32 v27, v26
	s_nop 0
	v_mul_f32_e32 v12, v12, v27
	v_mul_f32_e32 v27, 0xbfb8aa3b, v6
	v_pk_mul_f32 v[20:21], v[142:143], s[30:31] op_sel_hi:[1,0]
	v_exp_f32_e32 v27, v27
	v_mul_f32_e32 v12, v12, v20
	v_add_f32_e32 v27, 1.0, v27
	v_mul_f32_e32 v26, 0xbfb8aa3b, v7
	v_rcp_f32_e32 v20, v29
	s_nop 0
	v_mul_f32_e32 v13, v13, v20
	v_exp_f32_e32 v26, v26
	v_mul_f32_e32 v13, v13, v21
	v_add_f32_e32 v26, 1.0, v26
	v_pk_mul_f32 v[18:19], v[144:145], s[30:31] op_sel_hi:[1,0]
	v_rcp_f32_e32 v20, v27
	s_nop 0
	v_mul_f32_e32 v6, v6, v20
	v_mul_f32_e32 v18, v6, v18
	v_pk_mul_f32 v[16:17], v[170:171], s[28:29] op_sel_hi:[1,0]
	v_rcp_f32_e32 v6, v26
	s_nop 0
	v_mul_f32_e32 v6, v7, v6
	v_mul_f32_e32 v7, v6, v19
	v_mul_f32_e32 v6, 0xbfb8aa3b, v16
	v_exp_f32_e32 v19, v6
	v_med3_f32 v12, v12, s75, v239
	v_med3_f32 v13, v13, s75, v239
	v_mov_b32_e32 v6, v203
	v_cvt_pk_fp8_f32 v6, v12, v13
	v_add_f32_e32 v12, 1.0, v19
	v_med3_f32 v18, v18, s75, v239
	v_med3_f32 v7, v7, s75, v239
	v_cvt_pk_fp8_f32 v6, v18, v7 op_sel:[0,0,1]
	v_mul_f32_e32 v20, 0xbfb8aa3b, v17
	v_exp_f32_e32 v20, v20
	s_nop 0
	v_add_f32_e32 v13, 1.0, v20
	v_pk_mul_f32 v[14:15], v[172:173], s[28:29] op_sel_hi:[1,0]
	v_mul_f32_e32 v18, 0xbfb8aa3b, v14
	v_exp_f32_e32 v18, v18
	v_rcp_f32_e32 v7, v12
	s_nop 0
	v_mul_f32_e32 v7, v16, v7
	v_add_f32_e32 v18, 1.0, v18
	v_rcp_f32_e32 v12, v13
	s_nop 0
	v_mul_f32_e32 v12, v17, v12
	v_mul_f32_e32 v17, 0xbfb8aa3b, v15
	v_exp_f32_e32 v17, v17
	s_nop 0
	v_add_f32_e32 v17, 1.0, v17
	v_rcp_f32_e32 v13, v18
	s_nop 0
	v_mul_f32_e32 v13, v14, v13
	v_pk_mul_f32 v[24:25], v[138:139], s[30:31] op_sel_hi:[1,0]
	v_mul_f32_e32 v7, v7, v24
	v_mul_f32_e32 v12, v12, v25
	v_pk_mul_f32 v[22:23], v[140:141], s[30:31] op_sel_hi:[1,0]
	v_rcp_f32_e32 v14, v17
	s_nop 0
	v_mul_f32_e32 v14, v15, v14
	v_med3_f32 v15, v7, s75, v239
	v_med3_f32 v12, v12, s75, v239
	v_mov_b32_e32 v7, v203
	v_cvt_pk_fp8_f32 v7, v15, v12
	v_mul_f32_e32 v12, v14, v23
	v_pk_mul_f32 v[14:15], v[166:167], s[28:29] op_sel_hi:[1,0]
	v_mul_f32_e32 v13, v13, v22
	v_mul_f32_e32 v16, 0xbfb8aa3b, v14
	v_exp_f32_e32 v22, v16
	v_mul_f32_e32 v33, 0xbfb8aa3b, v15
	v_exp_f32_e32 v33, v33
	v_med3_f32 v13, v13, s75, v239
	v_add_f32_e32 v28, 1.0, v22
	v_med3_f32 v12, v12, s75, v239
	v_cvt_pk_fp8_f32 v7, v13, v12 op_sel:[0,0,1]
	v_pk_mul_f32 v[12:13], v[168:169], s[28:29] op_sel_hi:[1,0]
	s_waitcnt lgkmcnt(0)
	v_add_f32_e32 v31, 1.0, v33
	v_rcp_f32_e32 v29, v28
	s_nop 0
	v_mul_f32_e32 v14, v14, v29
	v_mul_f32_e32 v29, 0xbfb8aa3b, v12
	v_pk_mul_f32 v[22:23], v[134:135], s[30:31] op_sel_hi:[1,0]
	v_exp_f32_e32 v29, v29
	v_mul_f32_e32 v14, v14, v22
	v_add_f32_e32 v29, 1.0, v29
	v_mul_f32_e32 v28, 0xbfb8aa3b, v13
	v_rcp_f32_e32 v22, v31
	s_nop 0
	v_mul_f32_e32 v15, v15, v22
	v_exp_f32_e32 v28, v28
	v_mul_f32_e32 v15, v15, v23
	v_add_f32_e32 v28, 1.0, v28
	v_pk_mul_f32 v[20:21], v[136:137], s[30:31] op_sel_hi:[1,0]
	v_rcp_f32_e32 v22, v29
	s_nop 0
	v_mul_f32_e32 v12, v12, v22
	v_mul_f32_e32 v20, v12, v20
	v_pk_mul_f32 v[18:19], v[162:163], s[28:29] op_sel_hi:[1,0]
	v_rcp_f32_e32 v12, v28
	s_nop 0
	v_mul_f32_e32 v12, v13, v12
	v_mul_f32_e32 v13, v12, v21
	v_mul_f32_e32 v12, 0xbfb8aa3b, v18
	v_exp_f32_e32 v21, v12
	v_med3_f32 v14, v14, s75, v239
	v_med3_f32 v15, v15, s75, v239
	v_mov_b32_e32 v12, v203
	v_cvt_pk_fp8_f32 v12, v14, v15
	v_add_f32_e32 v14, 1.0, v21
	v_med3_f32 v20, v20, s75, v239
	v_med3_f32 v13, v13, s75, v239
	v_cvt_pk_fp8_f32 v12, v20, v13 op_sel:[0,0,1]
	v_mul_f32_e32 v22, 0xbfb8aa3b, v19
	v_exp_f32_e32 v22, v22
	s_nop 0
	v_add_f32_e32 v15, 1.0, v22
	v_pk_mul_f32 v[16:17], v[164:165], s[28:29] op_sel_hi:[1,0]
	v_mul_f32_e32 v20, 0xbfb8aa3b, v16
	v_exp_f32_e32 v20, v20
	v_rcp_f32_e32 v13, v14
	s_nop 0
	v_mul_f32_e32 v13, v18, v13
	v_add_f32_e32 v20, 1.0, v20
	v_rcp_f32_e32 v14, v15
	s_nop 0
	v_mul_f32_e32 v14, v19, v14
	v_mul_f32_e32 v19, 0xbfb8aa3b, v17
	v_exp_f32_e32 v19, v19
	s_nop 0
	v_add_f32_e32 v19, 1.0, v19
	v_rcp_f32_e32 v15, v20
	s_nop 0
	v_mul_f32_e32 v15, v16, v15
	v_pk_mul_f32 v[26:27], v[130:131], s[30:31] op_sel_hi:[1,0]
	v_mul_f32_e32 v13, v13, v26
	v_mul_f32_e32 v14, v14, v27
	v_rcp_f32_e32 v16, v19
	s_nop 0
	v_mul_f32_e32 v16, v17, v16
	v_med3_f32 v17, v13, s75, v239
	v_med3_f32 v14, v14, s75, v239
	v_mov_b32_e32 v13, v203
	v_cvt_pk_fp8_f32 v13, v17, v14
	ds_write_b64 v8, v[2:3]
	ds_write_b64 v8, v[4:5] offset:512
	v_pk_mul_f32 v[24:25], v[132:133], s[30:31] op_sel_hi:[1,0]
	ds_read_b128 v[2:5], v9
	v_mul_f32_e32 v15, v15, v24
	v_mul_f32_e32 v14, v16, v25
	v_med3_f32 v15, v15, s75, v239
	v_med3_f32 v14, v14, s75, v239
	v_cvt_pk_fp8_f32 v13, v15, v14 op_sel:[0,0,1]
	v_lshl_add_u32 v10, v10, 9, v11
	s_waitcnt lgkmcnt(0)
	global_store_dwordx4 v10, v[2:5], s[16:17] nt
	ds_write_b64 v8, v[6:7] offset:1024
	ds_write_b64 v8, v[12:13] offset:1536
	v_pk_mul_f32 v[12:13], v[126:127], s[28:29] op_sel_hi:[1,0]
	v_pk_mul_f32 v[6:7], v[128:129], s[28:29] op_sel_hi:[1,0]
	v_mul_f32_e32 v11, 0xbfb8aa3b, v12
	v_exp_f32_e32 v11, v11
	v_mul_f32_e32 v30, 0xbfb8aa3b, v13
	v_exp_f32_e32 v30, v30
	v_pk_mul_f32 v[20:21], v[94:95], s[30:31] op_sel_hi:[1,0]
	v_add_f32_e32 v11, 1.0, v11
	v_pk_mul_f32 v[18:19], v[96:97], s[30:31] op_sel_hi:[1,0]
	v_pk_mul_f32 v[16:17], v[122:123], s[28:29] op_sel_hi:[1,0]
	v_pk_mul_f32 v[14:15], v[124:125], s[28:29] op_sel_hi:[1,0]
	v_add_f32_e32 v28, 1.0, v30
	v_rcp_f32_e32 v11, v11
	s_nop 0
	v_mul_f32_e32 v11, v12, v11
	v_mul_f32_e32 v26, 0xbfb8aa3b, v6
	v_exp_f32_e32 v26, v26
	v_mul_f32_e32 v11, v20, v11
	v_add_f32_e32 v26, 1.0, v26
	v_rcp_f32_e32 v12, v28
	s_nop 0
	v_mul_f32_e32 v12, v13, v12
	v_mul_f32_e32 v12, v21, v12
	v_mul_f32_e32 v21, 0xbfb8aa3b, v7
	v_exp_f32_e32 v21, v21
	s_nop 0
	v_add_f32_e32 v21, 1.0, v21
	v_rcp_f32_e32 v13, v26
	s_nop 0
	v_mul_f32_e32 v6, v6, v13
	v_mul_f32_e32 v13, v18, v6
	v_rcp_f32_e32 v6, v21
	s_nop 0
	v_mul_f32_e32 v6, v7, v6
	v_mul_f32_e32 v7, v19, v6
	v_mul_f32_e32 v6, 0xbfb8aa3b, v16
	v_exp_f32_e32 v18, v6
	v_med3_f32 v11, v11, s75, v239
	v_med3_f32 v12, v12, s75, v239
	v_mov_b32_e32 v6, v203
	v_cvt_pk_fp8_f32 v6, v11, v12
	v_add_f32_e32 v11, 1.0, v18
	v_med3_f32 v13, v13, s75, v239
	v_med3_f32 v7, v7, s75, v239
	v_cvt_pk_fp8_f32 v6, v13, v7 op_sel:[0,0,1]
	v_mul_f32_e32 v19, 0xbfb8aa3b, v17
	v_exp_f32_e32 v19, v19
	s_nop 0
	v_add_f32_e32 v12, 1.0, v19
	v_rcp_f32_e32 v7, v11
	s_nop 0
	v_mul_f32_e32 v7, v16, v7
	v_mul_f32_e32 v16, 0xbfb8aa3b, v14
	v_exp_f32_e32 v16, v16
	s_nop 0
	v_add_f32_e32 v16, 1.0, v16
	v_rcp_f32_e32 v11, v12
	s_nop 0
	v_mul_f32_e32 v11, v17, v11
	v_mul_f32_e32 v17, 0xbfb8aa3b, v15
	v_exp_f32_e32 v17, v17
	s_nop 0
	v_add_f32_e32 v17, 1.0, v17
	v_rcp_f32_e32 v12, v16
	s_nop 0
	v_mul_f32_e32 v12, v14, v12
	v_pk_mul_f32 v[24:25], v[90:91], s[30:31] op_sel_hi:[1,0]
	v_mul_f32_e32 v7, v24, v7
	v_mul_f32_e32 v11, v25, v11
	v_med3_f32 v14, v7, s75, v239
	v_med3_f32 v11, v11, s75, v239
	v_mov_b32_e32 v7, v203
	v_cvt_pk_fp8_f32 v7, v14, v11
	v_pk_mul_f32 v[22:23], v[92:93], s[30:31] op_sel_hi:[1,0]
	v_rcp_f32_e32 v13, v17
	s_nop 0
	v_mul_f32_e32 v13, v15, v13
	v_mul_f32_e32 v12, v22, v12
	v_mul_f32_e32 v11, v23, v13
	v_med3_f32 v12, v12, s75, v239
	v_med3_f32 v11, v11, s75, v239
	v_pk_mul_f32 v[14:15], v[118:119], s[28:29] op_sel_hi:[1,0]
	v_cvt_pk_fp8_f32 v7, v12, v11 op_sel:[0,0,1]
	v_mul_f32_e32 v11, 0xbfb8aa3b, v14
	v_exp_f32_e32 v11, v11
	v_mul_f32_e32 v32, 0xbfb8aa3b, v15
	v_exp_f32_e32 v32, v32
	v_pk_mul_f32 v[12:13], v[120:121], s[28:29] op_sel_hi:[1,0]
	v_add_f32_e32 v11, 1.0, v11
	v_pk_mul_f32 v[22:23], v[86:87], s[30:31] op_sel_hi:[1,0]
	v_pk_mul_f32 v[20:21], v[88:89], s[30:31] op_sel_hi:[1,0]
	v_pk_mul_f32 v[18:19], v[114:115], s[28:29] op_sel_hi:[1,0]
	v_add_f32_e32 v30, 1.0, v32
	v_rcp_f32_e32 v11, v11
	s_nop 0
	v_mul_f32_e32 v11, v14, v11
	v_mul_f32_e32 v28, 0xbfb8aa3b, v12
	v_exp_f32_e32 v28, v28
	v_mul_f32_e32 v11, v22, v11
	v_add_f32_e32 v28, 1.0, v28
	v_rcp_f32_e32 v14, v30
	s_nop 0
	v_mul_f32_e32 v14, v15, v14
	v_mul_f32_e32 v14, v23, v14
	v_mul_f32_e32 v23, 0xbfb8aa3b, v13
	v_exp_f32_e32 v23, v23
	s_nop 0
	v_add_f32_e32 v23, 1.0, v23
	v_rcp_f32_e32 v15, v28
	s_nop 0
	v_mul_f32_e32 v12, v12, v15
	v_mul_f32_e32 v15, v20, v12
	v_rcp_f32_e32 v12, v23
	s_nop 0
	v_mul_f32_e32 v12, v13, v12
	v_mul_f32_e32 v13, v21, v12
	v_mul_f32_e32 v12, 0xbfb8aa3b, v18
	v_exp_f32_e32 v20, v12
	v_med3_f32 v11, v11, s75, v239
	v_med3_f32 v14, v14, s75, v239
	v_mov_b32_e32 v12, v203
	v_cvt_pk_fp8_f32 v12, v11, v14
	v_add_f32_e32 v11, 1.0, v20
	v_med3_f32 v15, v15, s75, v239
	v_med3_f32 v13, v13, s75, v239
	v_cvt_pk_fp8_f32 v12, v15, v13 op_sel:[0,0,1]
	v_mul_f32_e32 v21, 0xbfb8aa3b, v19
	v_exp_f32_e32 v21, v21
	s_nop 0
	v_add_f32_e32 v14, 1.0, v21
	v_pk_mul_f32 v[16:17], v[116:117], s[28:29] op_sel_hi:[1,0]
	v_rcp_f32_e32 v11, v11
	s_nop 0
	v_mul_f32_e32 v11, v18, v11
	v_mul_f32_e32 v18, 0xbfb8aa3b, v16
	v_exp_f32_e32 v18, v18
	s_nop 0
	v_add_f32_e32 v18, 1.0, v18
	v_rcp_f32_e32 v13, v14
	s_nop 0
	v_mul_f32_e32 v13, v19, v13
	v_mul_f32_e32 v19, 0xbfb8aa3b, v17
	v_exp_f32_e32 v19, v19
	s_nop 0
	v_add_f32_e32 v19, 1.0, v19
	v_rcp_f32_e32 v14, v18
	s_nop 0
	v_mul_f32_e32 v14, v16, v14
	v_pk_mul_f32 v[26:27], v[82:83], s[30:31] op_sel_hi:[1,0]
	v_mul_f32_e32 v11, v26, v11
	v_mul_f32_e32 v13, v27, v13
	v_med3_f32 v11, v11, s75, v239
	v_med3_f32 v16, v13, s75, v239
	v_mov_b32_e32 v13, v203
	v_cvt_pk_fp8_f32 v13, v11, v16
	v_pk_mul_f32 v[24:25], v[84:85], s[30:31] op_sel_hi:[1,0]
	v_rcp_f32_e32 v15, v19
	s_nop 0
	v_mul_f32_e32 v15, v17, v15
	ds_read_b128 v[2:5], v9 offset:1024
	v_mul_f32_e32 v14, v24, v14
	v_mul_f32_e32 v11, v25, v15
	v_med3_f32 v14, v14, s75, v239
	v_med3_f32 v11, v11, s75, v239
	v_cvt_pk_fp8_f32 v13, v14, v11 op_sel:[0,0,1]
	v_add_u32_e32 v11, 0x4000, v10
	s_waitcnt lgkmcnt(0)
	global_store_dwordx4 v11, v[2:5], s[16:17] nt
	ds_write_b64 v8, v[6:7]
	ds_write_b64 v8, v[12:13] offset:512
	v_pk_mul_f32 v[12:13], v[110:111], s[28:29] op_sel_hi:[1,0]
	v_pk_mul_f32 v[6:7], v[112:113], s[28:29] op_sel_hi:[1,0]
	v_mul_f32_e32 v11, 0xbfb8aa3b, v12
	v_exp_f32_e32 v11, v11
	v_mul_f32_e32 v30, 0xbfb8aa3b, v13
	v_exp_f32_e32 v30, v30
	v_pk_mul_f32 v[20:21], v[78:79], s[30:31] op_sel_hi:[1,0]
	v_add_f32_e32 v11, 1.0, v11
	v_pk_mul_f32 v[18:19], v[80:81], s[30:31] op_sel_hi:[1,0]
	v_pk_mul_f32 v[16:17], v[106:107], s[28:29] op_sel_hi:[1,0]
	v_pk_mul_f32 v[14:15], v[108:109], s[28:29] op_sel_hi:[1,0]
	v_add_f32_e32 v28, 1.0, v30
	v_rcp_f32_e32 v11, v11
	s_nop 0
	v_mul_f32_e32 v11, v12, v11
	v_mul_f32_e32 v26, 0xbfb8aa3b, v6
	v_exp_f32_e32 v26, v26
	v_mul_f32_e32 v11, v20, v11
	v_add_f32_e32 v26, 1.0, v26
	v_rcp_f32_e32 v12, v28
	s_nop 0
	v_mul_f32_e32 v12, v13, v12
	v_mul_f32_e32 v12, v21, v12
	v_mul_f32_e32 v21, 0xbfb8aa3b, v7
	v_exp_f32_e32 v21, v21
	s_nop 0
	v_add_f32_e32 v21, 1.0, v21
	v_rcp_f32_e32 v13, v26
	s_nop 0
	v_mul_f32_e32 v6, v6, v13
	v_mul_f32_e32 v13, v18, v6
	v_rcp_f32_e32 v6, v21
	s_nop 0
	v_mul_f32_e32 v6, v7, v6
	v_mul_f32_e32 v7, v19, v6
	v_mul_f32_e32 v6, 0xbfb8aa3b, v16
	v_exp_f32_e32 v18, v6
	v_med3_f32 v11, v11, s75, v239
	v_med3_f32 v12, v12, s75, v239
	v_mov_b32_e32 v6, v203
	v_cvt_pk_fp8_f32 v6, v11, v12
	v_add_f32_e32 v11, 1.0, v18
	v_med3_f32 v13, v13, s75, v239
	v_med3_f32 v7, v7, s75, v239
	v_cvt_pk_fp8_f32 v6, v13, v7 op_sel:[0,0,1]
	v_mul_f32_e32 v19, 0xbfb8aa3b, v17
	v_exp_f32_e32 v19, v19
	s_nop 0
	v_add_f32_e32 v12, 1.0, v19
	v_rcp_f32_e32 v7, v11
	s_nop 0
	v_mul_f32_e32 v7, v16, v7
	v_mul_f32_e32 v16, 0xbfb8aa3b, v14
	v_exp_f32_e32 v16, v16
	s_nop 0
	v_add_f32_e32 v16, 1.0, v16
	v_rcp_f32_e32 v11, v12
	s_nop 0
	v_mul_f32_e32 v11, v17, v11
	v_mul_f32_e32 v17, 0xbfb8aa3b, v15
	v_exp_f32_e32 v17, v17
	s_nop 0
	v_add_f32_e32 v17, 1.0, v17
	v_rcp_f32_e32 v12, v16
	s_nop 0
	v_mul_f32_e32 v12, v14, v12
	v_pk_mul_f32 v[24:25], v[74:75], s[30:31] op_sel_hi:[1,0]
	v_mul_f32_e32 v7, v24, v7
	v_mul_f32_e32 v11, v25, v11
	v_med3_f32 v14, v7, s75, v239
	v_med3_f32 v11, v11, s75, v239
	v_mov_b32_e32 v7, v203
	v_cvt_pk_fp8_f32 v7, v14, v11
	v_pk_mul_f32 v[22:23], v[76:77], s[30:31] op_sel_hi:[1,0]
	v_rcp_f32_e32 v13, v17
	s_nop 0
	v_mul_f32_e32 v13, v15, v13
	v_mul_f32_e32 v12, v22, v12
	v_mul_f32_e32 v11, v23, v13
	v_med3_f32 v12, v12, s75, v239
	v_med3_f32 v11, v11, s75, v239
	v_pk_mul_f32 v[14:15], v[102:103], s[28:29] op_sel_hi:[1,0]
	v_cvt_pk_fp8_f32 v7, v12, v11 op_sel:[0,0,1]
	v_mul_f32_e32 v11, 0xbfb8aa3b, v14
	v_exp_f32_e32 v11, v11
	v_mul_f32_e32 v32, 0xbfb8aa3b, v15
	v_exp_f32_e32 v32, v32
	v_pk_mul_f32 v[12:13], v[104:105], s[28:29] op_sel_hi:[1,0]
	v_add_f32_e32 v11, 1.0, v11
	v_pk_mul_f32 v[22:23], v[70:71], s[30:31] op_sel_hi:[1,0]
	v_pk_mul_f32 v[20:21], v[72:73], s[30:31] op_sel_hi:[1,0]
	v_pk_mul_f32 v[18:19], v[98:99], s[28:29] op_sel_hi:[1,0]
	v_add_f32_e32 v30, 1.0, v32
	v_rcp_f32_e32 v11, v11
	s_nop 0
	v_mul_f32_e32 v11, v14, v11
	v_mul_f32_e32 v28, 0xbfb8aa3b, v12
	v_exp_f32_e32 v28, v28
	v_mul_f32_e32 v11, v22, v11
	v_add_f32_e32 v28, 1.0, v28
	v_rcp_f32_e32 v14, v30
	s_nop 0
	v_mul_f32_e32 v14, v15, v14
	v_mul_f32_e32 v14, v23, v14
	v_mul_f32_e32 v23, 0xbfb8aa3b, v13
	v_exp_f32_e32 v23, v23
	s_nop 0
	v_add_f32_e32 v23, 1.0, v23
	v_rcp_f32_e32 v15, v28
	s_nop 0
	v_mul_f32_e32 v12, v12, v15
	v_mul_f32_e32 v15, v20, v12
	v_rcp_f32_e32 v12, v23
	s_nop 0
	v_mul_f32_e32 v12, v13, v12
	v_mul_f32_e32 v13, v21, v12
	v_mul_f32_e32 v12, 0xbfb8aa3b, v18
	v_exp_f32_e32 v20, v12
	v_med3_f32 v11, v11, s75, v239
	v_med3_f32 v14, v14, s75, v239
	v_mov_b32_e32 v12, v203
	v_cvt_pk_fp8_f32 v12, v11, v14
	v_add_f32_e32 v11, 1.0, v20
	v_med3_f32 v15, v15, s75, v239
	v_med3_f32 v13, v13, s75, v239
	v_cvt_pk_fp8_f32 v12, v15, v13 op_sel:[0,0,1]
	v_mul_f32_e32 v21, 0xbfb8aa3b, v19
	v_exp_f32_e32 v21, v21
	s_nop 0
	v_add_f32_e32 v14, 1.0, v21
	v_pk_mul_f32 v[16:17], v[100:101], s[28:29] op_sel_hi:[1,0]
	v_rcp_f32_e32 v11, v11
	s_nop 0
	v_mul_f32_e32 v11, v18, v11
	v_mul_f32_e32 v18, 0xbfb8aa3b, v16
	v_exp_f32_e32 v18, v18
	s_nop 0
	v_add_f32_e32 v18, 1.0, v18
	v_rcp_f32_e32 v13, v14
	s_nop 0
	v_mul_f32_e32 v13, v19, v13
	v_mul_f32_e32 v19, 0xbfb8aa3b, v17
	v_exp_f32_e32 v19, v19
	s_nop 0
	v_add_f32_e32 v19, 1.0, v19
	v_rcp_f32_e32 v14, v18
	s_nop 0
	v_mul_f32_e32 v14, v16, v14
	v_pk_mul_f32 v[26:27], v[66:67], s[30:31] op_sel_hi:[1,0]
	v_mul_f32_e32 v11, v26, v11
	v_mul_f32_e32 v13, v27, v13
	v_med3_f32 v11, v11, s75, v239
	v_med3_f32 v16, v13, s75, v239
	v_mov_b32_e32 v13, v203
	v_cvt_pk_fp8_f32 v13, v11, v16
	v_pk_mul_f32 v[24:25], v[68:69], s[30:31] op_sel_hi:[1,0]
	v_rcp_f32_e32 v15, v19
	s_nop 0
	v_mul_f32_e32 v15, v17, v15
	ds_read_b128 v[2:5], v9
	v_mul_f32_e32 v14, v24, v14
	v_mul_f32_e32 v11, v25, v15
	v_med3_f32 v14, v14, s75, v239
	v_med3_f32 v11, v11, s75, v239
	v_cvt_pk_fp8_f32 v13, v14, v11 op_sel:[0,0,1]
	v_add_u32_e32 v11, 0x10000, v10
	s_waitcnt lgkmcnt(0)
	global_store_dwordx4 v11, v[2:5], s[16:17] nt
	ds_write_b64 v8, v[6:7] offset:1024
	ds_write_b64 v8, v[12:13] offset:1536
	ds_read_b128 v[2:5], v9 offset:1024
	v_add_u32_e32 v6, 0x14000, v10
	s_andn2_b64 vcc, exec, s[42:43]
	s_waitcnt lgkmcnt(0)
	global_store_dwordx4 v6, v[2:5], s[16:17] nt
	s_cbranch_vccnz .LBB0_1680
	s_andn2_b64 vcc, exec, s[20:21]
	s_cbranch_vccnz .LBB0_1647
	s_barrier
	s_branch .LBB0_1647

.LBB0_1853:
	v_mov_b32_e32 v2, v232
	s_add_u32 s0, s79, 0xffffff00
	s_nop 15
	s_nop 15
	s_nop 15
	s_addc_u32 s1, s80, -1
	v_lshlrev_b32_e32 v3, 5, v2
	v_ashrrev_i32_e32 v4, 1, v2
	v_and_b32_e32 v3, 0x1e0, v3
	v_and_b32_e32 v5, -8, v4
	s_add_i32 s2, s33, s69
	v_add3_u32 v8, s53, v3, v5
	v_add_u32_e32 v10, s2, v4
	v_pk_mul_f32 v[4:5], v[190:191], s[28:29] op_sel_hi:[1,0]
	v_lshlrev_b32_e32 v2, 4, v2
	v_mul_f32_e32 v6, 0xbfb8aa3b, v4
	v_exp_f32_e32 v16, v6
	v_mul_f32_e32 v27, 0xbfb8aa3b, v5
	v_exp_f32_e32 v27, v27
	v_add_u32_e32 v9, s53, v2
	v_add_f32_e32 v22, 1.0, v16
	v_and_b32_e32 v11, 16, v2
	v_pk_mul_f32 v[2:3], v[192:193], s[28:29] op_sel_hi:[1,0]
	v_pk_mul_f32 v[16:17], v[158:159], s[30:31] op_sel_hi:[1,0]
	v_add_f32_e32 v25, 1.0, v27
	v_rcp_f32_e32 v23, v22
	s_nop 0
	v_mul_f32_e32 v4, v4, v23
	v_mul_f32_e32 v23, 0xbfb8aa3b, v2
	v_exp_f32_e32 v23, v23
	v_mul_f32_e32 v4, v4, v16
	v_add_f32_e32 v23, 1.0, v23
	v_mul_f32_e32 v22, 0xbfb8aa3b, v3
	v_rcp_f32_e32 v16, v25
	s_nop 0
	v_mul_f32_e32 v5, v5, v16
	v_exp_f32_e32 v22, v22
	v_mul_f32_e32 v5, v5, v17
	v_add_f32_e32 v22, 1.0, v22
	v_pk_mul_f32 v[14:15], v[160:161], s[30:31] op_sel_hi:[1,0]
	v_rcp_f32_e32 v16, v23
	s_nop 0
	v_mul_f32_e32 v2, v2, v16
	v_mul_f32_e32 v14, v2, v14
	v_pk_mul_f32 v[12:13], v[186:187], s[28:29] op_sel_hi:[1,0]
	v_rcp_f32_e32 v2, v22
	s_nop 0
	v_mul_f32_e32 v2, v3, v2
	v_mul_f32_e32 v3, v2, v15
	v_mul_f32_e32 v2, 0xbfb8aa3b, v12
	v_exp_f32_e32 v15, v2
	v_med3_f32 v4, v4, s75, v233
	v_med3_f32 v5, v5, s75, v233
	v_mov_b32_e32 v2, v203
	v_cvt_pk_fp8_f32 v2, v4, v5
	v_add_f32_e32 v4, 1.0, v15
	v_med3_f32 v14, v14, s75, v233
	v_med3_f32 v3, v3, s75, v233
	v_cvt_pk_fp8_f32 v2, v14, v3 op_sel:[0,0,1]
	v_mul_f32_e32 v16, 0xbfb8aa3b, v13
	v_exp_f32_e32 v16, v16
	s_nop 0
	v_add_f32_e32 v5, 1.0, v16
	v_pk_mul_f32 v[6:7], v[188:189], s[28:29] op_sel_hi:[1,0]
	v_mul_f32_e32 v14, 0xbfb8aa3b, v6
	v_exp_f32_e32 v14, v14
	v_rcp_f32_e32 v3, v4
	s_nop 0
	v_mul_f32_e32 v3, v12, v3
	v_add_f32_e32 v14, 1.0, v14
	v_rcp_f32_e32 v4, v5
	s_nop 0
	v_mul_f32_e32 v4, v13, v4
	v_mul_f32_e32 v13, 0xbfb8aa3b, v7
	v_exp_f32_e32 v13, v13
	s_nop 0
	v_add_f32_e32 v13, 1.0, v13
	v_rcp_f32_e32 v5, v14
	s_nop 0
	v_mul_f32_e32 v5, v6, v5
	v_pk_mul_f32 v[20:21], v[154:155], s[30:31] op_sel_hi:[1,0]
	v_mul_f32_e32 v3, v3, v20
	v_mul_f32_e32 v4, v4, v21
	v_pk_mul_f32 v[18:19], v[156:157], s[30:31] op_sel_hi:[1,0]
	v_rcp_f32_e32 v6, v13
	s_nop 0
	v_mul_f32_e32 v6, v7, v6
	v_med3_f32 v7, v3, s75, v233
	v_med3_f32 v4, v4, s75, v233
	v_mov_b32_e32 v3, v203
	v_cvt_pk_fp8_f32 v3, v7, v4
	v_mul_f32_e32 v4, v6, v19
	v_pk_mul_f32 v[6:7], v[182:183], s[28:29] op_sel_hi:[1,0]
	v_mul_f32_e32 v5, v5, v18
	v_mul_f32_e32 v12, 0xbfb8aa3b, v6
	v_exp_f32_e32 v18, v12
	v_mul_f32_e32 v29, 0xbfb8aa3b, v7
	v_exp_f32_e32 v29, v29
	v_med3_f32 v5, v5, s75, v233
	v_add_f32_e32 v24, 1.0, v18
	v_med3_f32 v4, v4, s75, v233
	v_cvt_pk_fp8_f32 v3, v5, v4 op_sel:[0,0,1]
	v_pk_mul_f32 v[4:5], v[184:185], s[28:29] op_sel_hi:[1,0]
	v_add_f32_e32 v27, 1.0, v29
	v_rcp_f32_e32 v25, v24
	s_nop 0
	v_mul_f32_e32 v6, v6, v25
	v_mul_f32_e32 v25, 0xbfb8aa3b, v4
	v_pk_mul_f32 v[18:19], v[150:151], s[30:31] op_sel_hi:[1,0]
	v_exp_f32_e32 v25, v25
	v_mul_f32_e32 v6, v6, v18
	v_add_f32_e32 v25, 1.0, v25
	v_mul_f32_e32 v24, 0xbfb8aa3b, v5
	v_rcp_f32_e32 v18, v27
	s_nop 0
	v_mul_f32_e32 v7, v7, v18
	v_exp_f32_e32 v24, v24
	v_mul_f32_e32 v7, v7, v19
	v_add_f32_e32 v24, 1.0, v24
	v_pk_mul_f32 v[16:17], v[152:153], s[30:31] op_sel_hi:[1,0]
	v_rcp_f32_e32 v18, v25
	s_nop 0
	v_mul_f32_e32 v4, v4, v18
	v_mul_f32_e32 v16, v4, v16
	v_pk_mul_f32 v[14:15], v[178:179], s[28:29] op_sel_hi:[1,0]
	v_rcp_f32_e32 v4, v24
	s_nop 0
	v_mul_f32_e32 v4, v5, v4
	v_mul_f32_e32 v5, v4, v17
	v_mul_f32_e32 v4, 0xbfb8aa3b, v14
	v_exp_f32_e32 v17, v4
	v_med3_f32 v6, v6, s75, v233
	v_med3_f32 v7, v7, s75, v233
	v_mov_b32_e32 v4, v203
	v_cvt_pk_fp8_f32 v4, v6, v7
	v_add_f32_e32 v6, 1.0, v17
	v_med3_f32 v16, v16, s75, v233
	v_med3_f32 v5, v5, s75, v233
	v_cvt_pk_fp8_f32 v4, v16, v5 op_sel:[0,0,1]
	v_mul_f32_e32 v18, 0xbfb8aa3b, v15
	v_exp_f32_e32 v18, v18
	s_nop 0
	v_add_f32_e32 v7, 1.0, v18
	v_pk_mul_f32 v[12:13], v[180:181], s[28:29] op_sel_hi:[1,0]
	v_mul_f32_e32 v16, 0xbfb8aa3b, v12
	v_exp_f32_e32 v16, v16
	v_rcp_f32_e32 v5, v6
	s_nop 0
	v_mul_f32_e32 v5, v14, v5
	v_add_f32_e32 v16, 1.0, v16
	v_rcp_f32_e32 v6, v7
	s_nop 0
	v_mul_f32_e32 v6, v15, v6
	v_mul_f32_e32 v15, 0xbfb8aa3b, v13
	v_exp_f32_e32 v15, v15
	s_nop 0
	v_add_f32_e32 v15, 1.0, v15
	v_rcp_f32_e32 v7, v16
	s_nop 0
	v_mul_f32_e32 v7, v12, v7
	v_pk_mul_f32 v[22:23], v[146:147], s[30:31] op_sel_hi:[1,0]
	v_mul_f32_e32 v5, v5, v22
	v_mul_f32_e32 v6, v6, v23
	v_pk_mul_f32 v[20:21], v[148:149], s[30:31] op_sel_hi:[1,0]
	v_rcp_f32_e32 v12, v15
	s_nop 0
	v_mul_f32_e32 v12, v13, v12
	v_med3_f32 v13, v5, s75, v233
	v_med3_f32 v6, v6, s75, v233
	v_mov_b32_e32 v5, v203
	v_cvt_pk_fp8_f32 v5, v13, v6
	v_mul_f32_e32 v6, v12, v21
	v_pk_mul_f32 v[12:13], v[174:175], s[28:29] op_sel_hi:[1,0]
	v_mul_f32_e32 v7, v7, v20
	v_mul_f32_e32 v14, 0xbfb8aa3b, v12
	v_exp_f32_e32 v20, v14
	v_mul_f32_e32 v31, 0xbfb8aa3b, v13
	v_exp_f32_e32 v31, v31
	v_med3_f32 v7, v7, s75, v233
	v_add_f32_e32 v26, 1.0, v20
	v_med3_f32 v6, v6, s75, v233
	v_cvt_pk_fp8_f32 v5, v7, v6 op_sel:[0,0,1]
	v_lshl_or_b32 v6, s18, 7, v11
	v_add_f32_e32 v29, 1.0, v31
	v_or_b32_e32 v11, s70, v6
	v_pk_mul_f32 v[6:7], v[176:177], s[28:29] op_sel_hi:[1,0]
	v_rcp_f32_e32 v27, v26
	s_nop 0
	v_mul_f32_e32 v12, v12, v27
	v_mul_f32_e32 v27, 0xbfb8aa3b, v6
	v_pk_mul_f32 v[20:21], v[142:143], s[30:31] op_sel_hi:[1,0]
	v_exp_f32_e32 v27, v27
	v_mul_f32_e32 v12, v12, v20
	v_add_f32_e32 v27, 1.0, v27
	v_mul_f32_e32 v26, 0xbfb8aa3b, v7
	v_rcp_f32_e32 v20, v29
	s_nop 0
	v_mul_f32_e32 v13, v13, v20
	v_exp_f32_e32 v26, v26
	v_mul_f32_e32 v13, v13, v21
	v_add_f32_e32 v26, 1.0, v26
	v_pk_mul_f32 v[18:19], v[144:145], s[30:31] op_sel_hi:[1,0]
	v_rcp_f32_e32 v20, v27
	s_nop 0
	v_mul_f32_e32 v6, v6, v20
	v_mul_f32_e32 v18, v6, v18
	v_pk_mul_f32 v[16:17], v[170:171], s[28:29] op_sel_hi:[1,0]
	v_rcp_f32_e32 v6, v26
	s_nop 0
	v_mul_f32_e32 v6, v7, v6
	v_mul_f32_e32 v7, v6, v19
	v_mul_f32_e32 v6, 0xbfb8aa3b, v16
	v_exp_f32_e32 v19, v6
	v_med3_f32 v12, v12, s75, v233
	v_med3_f32 v13, v13, s75, v233
	v_mov_b32_e32 v6, v203
	v_cvt_pk_fp8_f32 v6, v12, v13
	v_add_f32_e32 v12, 1.0, v19
	v_med3_f32 v18, v18, s75, v233
	v_med3_f32 v7, v7, s75, v233
	v_cvt_pk_fp8_f32 v6, v18, v7 op_sel:[0,0,1]
	v_mul_f32_e32 v20, 0xbfb8aa3b, v17
	v_exp_f32_e32 v20, v20
	s_nop 0
	v_add_f32_e32 v13, 1.0, v20
	v_pk_mul_f32 v[14:15], v[172:173], s[28:29] op_sel_hi:[1,0]
	v_mul_f32_e32 v18, 0xbfb8aa3b, v14
	v_exp_f32_e32 v18, v18
	v_rcp_f32_e32 v7, v12
	s_nop 0
	v_mul_f32_e32 v7, v16, v7
	v_add_f32_e32 v18, 1.0, v18
	v_rcp_f32_e32 v12, v13
	s_nop 0
	v_mul_f32_e32 v12, v17, v12
	v_mul_f32_e32 v17, 0xbfb8aa3b, v15
	v_exp_f32_e32 v17, v17
	s_nop 0
	v_add_f32_e32 v17, 1.0, v17
	v_rcp_f32_e32 v13, v18
	s_nop 0
	v_mul_f32_e32 v13, v14, v13
	v_pk_mul_f32 v[24:25], v[138:139], s[30:31] op_sel_hi:[1,0]
	v_mul_f32_e32 v7, v7, v24
	v_mul_f32_e32 v12, v12, v25
	v_pk_mul_f32 v[22:23], v[140:141], s[30:31] op_sel_hi:[1,0]
	v_rcp_f32_e32 v14, v17
	s_nop 0
	v_mul_f32_e32 v14, v15, v14
	v_med3_f32 v15, v7, s75, v233
	v_med3_f32 v12, v12, s75, v233
	v_mov_b32_e32 v7, v203
	v_cvt_pk_fp8_f32 v7, v15, v12
	v_mul_f32_e32 v12, v14, v23
	v_pk_mul_f32 v[14:15], v[166:167], s[28:29] op_sel_hi:[1,0]
	v_mul_f32_e32 v13, v13, v22
	v_mul_f32_e32 v16, 0xbfb8aa3b, v14
	v_exp_f32_e32 v22, v16
	v_mul_f32_e32 v33, 0xbfb8aa3b, v15
	v_exp_f32_e32 v33, v33
	v_med3_f32 v13, v13, s75, v233
	v_add_f32_e32 v28, 1.0, v22
	v_med3_f32 v12, v12, s75, v233
	v_cvt_pk_fp8_f32 v7, v13, v12 op_sel:[0,0,1]
	v_pk_mul_f32 v[12:13], v[168:169], s[28:29] op_sel_hi:[1,0]
	s_waitcnt lgkmcnt(0)
	v_add_f32_e32 v31, 1.0, v33
	v_rcp_f32_e32 v29, v28
	s_nop 0
	v_mul_f32_e32 v14, v14, v29
	v_mul_f32_e32 v29, 0xbfb8aa3b, v12
	v_pk_mul_f32 v[22:23], v[134:135], s[30:31] op_sel_hi:[1,0]
	v_exp_f32_e32 v29, v29
	v_mul_f32_e32 v14, v14, v22
	v_add_f32_e32 v29, 1.0, v29
	v_mul_f32_e32 v28, 0xbfb8aa3b, v13
	v_rcp_f32_e32 v22, v31
	s_nop 0
	v_mul_f32_e32 v15, v15, v22
	v_exp_f32_e32 v28, v28
	v_mul_f32_e32 v15, v15, v23
	v_add_f32_e32 v28, 1.0, v28
	v_pk_mul_f32 v[20:21], v[136:137], s[30:31] op_sel_hi:[1,0]
	v_rcp_f32_e32 v22, v29
	s_nop 0
	v_mul_f32_e32 v12, v12, v22
	v_mul_f32_e32 v20, v12, v20
	v_pk_mul_f32 v[18:19], v[162:163], s[28:29] op_sel_hi:[1,0]
	v_rcp_f32_e32 v12, v28
	s_nop 0
	v_mul_f32_e32 v12, v13, v12
	v_mul_f32_e32 v13, v12, v21
	v_mul_f32_e32 v12, 0xbfb8aa3b, v18
	v_exp_f32_e32 v21, v12
	v_med3_f32 v14, v14, s75, v233
	v_med3_f32 v15, v15, s75, v233
	v_mov_b32_e32 v12, v203
	v_cvt_pk_fp8_f32 v12, v14, v15
	v_add_f32_e32 v14, 1.0, v21
	v_med3_f32 v20, v20, s75, v233
	v_med3_f32 v13, v13, s75, v233
	v_cvt_pk_fp8_f32 v12, v20, v13 op_sel:[0,0,1]
	v_mul_f32_e32 v22, 0xbfb8aa3b, v19
	v_exp_f32_e32 v22, v22
	s_nop 0
	v_add_f32_e32 v15, 1.0, v22
	v_pk_mul_f32 v[16:17], v[164:165], s[28:29] op_sel_hi:[1,0]
	v_mul_f32_e32 v20, 0xbfb8aa3b, v16
	v_exp_f32_e32 v20, v20
	v_rcp_f32_e32 v13, v14
	s_nop 0
	v_mul_f32_e32 v13, v18, v13
	v_add_f32_e32 v20, 1.0, v20
	v_rcp_f32_e32 v14, v15
	s_nop 0
	v_mul_f32_e32 v14, v19, v14
	v_mul_f32_e32 v19, 0xbfb8aa3b, v17
	v_exp_f32_e32 v19, v19
	s_nop 0
	v_add_f32_e32 v19, 1.0, v19
	v_rcp_f32_e32 v15, v20
	s_nop 0
	v_mul_f32_e32 v15, v16, v15
	v_pk_mul_f32 v[26:27], v[130:131], s[30:31] op_sel_hi:[1,0]
	v_mul_f32_e32 v13, v13, v26
	v_mul_f32_e32 v14, v14, v27
	v_rcp_f32_e32 v16, v19
	s_nop 0
	v_mul_f32_e32 v16, v17, v16
	v_med3_f32 v17, v13, s75, v233
	v_med3_f32 v14, v14, s75, v233
	v_mov_b32_e32 v13, v203
	v_cvt_pk_fp8_f32 v13, v17, v14
	ds_write_b64 v8, v[2:3]
	ds_write_b64 v8, v[4:5] offset:512
	v_pk_mul_f32 v[24:25], v[132:133], s[30:31] op_sel_hi:[1,0]
	ds_read_b128 v[2:5], v9
	v_mul_f32_e32 v15, v15, v24
	v_mul_f32_e32 v14, v16, v25
	v_med3_f32 v15, v15, s75, v233
	v_med3_f32 v14, v14, s75, v233
	v_cvt_pk_fp8_f32 v13, v15, v14 op_sel:[0,0,1]
	v_lshl_add_u32 v10, v10, 9, v11
	s_waitcnt lgkmcnt(0)
	global_store_dwordx4 v10, v[2:5], s[16:17] nt
	ds_write_b64 v8, v[6:7] offset:1024
	ds_write_b64 v8, v[12:13] offset:1536
	v_pk_mul_f32 v[12:13], v[126:127], s[28:29] op_sel_hi:[1,0]
	v_pk_mul_f32 v[6:7], v[128:129], s[28:29] op_sel_hi:[1,0]
	v_mul_f32_e32 v11, 0xbfb8aa3b, v12
	v_exp_f32_e32 v11, v11
	v_mul_f32_e32 v30, 0xbfb8aa3b, v13
	v_exp_f32_e32 v30, v30
	v_pk_mul_f32 v[20:21], v[94:95], s[30:31] op_sel_hi:[1,0]
	v_add_f32_e32 v11, 1.0, v11
	v_pk_mul_f32 v[18:19], v[96:97], s[30:31] op_sel_hi:[1,0]
	v_pk_mul_f32 v[16:17], v[122:123], s[28:29] op_sel_hi:[1,0]
	v_pk_mul_f32 v[14:15], v[124:125], s[28:29] op_sel_hi:[1,0]
	v_add_f32_e32 v28, 1.0, v30
	v_rcp_f32_e32 v11, v11
	s_nop 0
	v_mul_f32_e32 v11, v12, v11
	v_mul_f32_e32 v26, 0xbfb8aa3b, v6
	v_exp_f32_e32 v26, v26
	v_mul_f32_e32 v11, v20, v11
	v_add_f32_e32 v26, 1.0, v26
	v_rcp_f32_e32 v12, v28
	s_nop 0
	v_mul_f32_e32 v12, v13, v12
	v_mul_f32_e32 v12, v21, v12
	v_mul_f32_e32 v21, 0xbfb8aa3b, v7
	v_exp_f32_e32 v21, v21
	s_nop 0
	v_add_f32_e32 v21, 1.0, v21
	v_rcp_f32_e32 v13, v26
	s_nop 0
	v_mul_f32_e32 v6, v6, v13
	v_mul_f32_e32 v13, v18, v6
	v_rcp_f32_e32 v6, v21
	s_nop 0
	v_mul_f32_e32 v6, v7, v6
	v_mul_f32_e32 v7, v19, v6
	v_mul_f32_e32 v6, 0xbfb8aa3b, v16
	v_exp_f32_e32 v18, v6
	v_med3_f32 v11, v11, s75, v233
	v_med3_f32 v12, v12, s75, v233
	v_mov_b32_e32 v6, v203
	v_cvt_pk_fp8_f32 v6, v11, v12
	v_add_f32_e32 v11, 1.0, v18
	v_med3_f32 v13, v13, s75, v233
	v_med3_f32 v7, v7, s75, v233
	v_cvt_pk_fp8_f32 v6, v13, v7 op_sel:[0,0,1]
	v_mul_f32_e32 v19, 0xbfb8aa3b, v17
	v_exp_f32_e32 v19, v19
	s_nop 0
	v_add_f32_e32 v12, 1.0, v19
	v_rcp_f32_e32 v7, v11
	s_nop 0
	v_mul_f32_e32 v7, v16, v7
	v_mul_f32_e32 v16, 0xbfb8aa3b, v14
	v_exp_f32_e32 v16, v16
	s_nop 0
	v_add_f32_e32 v16, 1.0, v16
	v_rcp_f32_e32 v11, v12
	s_nop 0
	v_mul_f32_e32 v11, v17, v11
	v_mul_f32_e32 v17, 0xbfb8aa3b, v15
	v_exp_f32_e32 v17, v17
	s_nop 0
	v_add_f32_e32 v17, 1.0, v17
	v_rcp_f32_e32 v12, v16
	s_nop 0
	v_mul_f32_e32 v12, v14, v12
	v_pk_mul_f32 v[24:25], v[90:91], s[30:31] op_sel_hi:[1,0]
	v_mul_f32_e32 v7, v24, v7
	v_mul_f32_e32 v11, v25, v11
	v_med3_f32 v14, v7, s75, v233
	v_med3_f32 v11, v11, s75, v233
	v_mov_b32_e32 v7, v203
	v_cvt_pk_fp8_f32 v7, v14, v11
	v_pk_mul_f32 v[22:23], v[92:93], s[30:31] op_sel_hi:[1,0]
	v_rcp_f32_e32 v13, v17
	s_nop 0
	v_mul_f32_e32 v13, v15, v13
	v_mul_f32_e32 v12, v22, v12
	v_mul_f32_e32 v11, v23, v13
	v_med3_f32 v12, v12, s75, v233
	v_med3_f32 v11, v11, s75, v233
	v_pk_mul_f32 v[14:15], v[118:119], s[28:29] op_sel_hi:[1,0]
	v_cvt_pk_fp8_f32 v7, v12, v11 op_sel:[0,0,1]
	v_mul_f32_e32 v11, 0xbfb8aa3b, v14
	v_exp_f32_e32 v11, v11
	v_mul_f32_e32 v32, 0xbfb8aa3b, v15
	v_exp_f32_e32 v32, v32
	v_pk_mul_f32 v[12:13], v[120:121], s[28:29] op_sel_hi:[1,0]
	v_add_f32_e32 v11, 1.0, v11
	v_pk_mul_f32 v[22:23], v[86:87], s[30:31] op_sel_hi:[1,0]
	v_pk_mul_f32 v[20:21], v[88:89], s[30:31] op_sel_hi:[1,0]
	v_pk_mul_f32 v[18:19], v[114:115], s[28:29] op_sel_hi:[1,0]
	v_add_f32_e32 v30, 1.0, v32
	v_rcp_f32_e32 v11, v11
	s_nop 0
	v_mul_f32_e32 v11, v14, v11
	v_mul_f32_e32 v28, 0xbfb8aa3b, v12
	v_exp_f32_e32 v28, v28
	v_mul_f32_e32 v11, v22, v11
	v_add_f32_e32 v28, 1.0, v28
	v_rcp_f32_e32 v14, v30
	s_nop 0
	v_mul_f32_e32 v14, v15, v14
	v_mul_f32_e32 v14, v23, v14
	v_mul_f32_e32 v23, 0xbfb8aa3b, v13
	v_exp_f32_e32 v23, v23
	s_nop 0
	v_add_f32_e32 v23, 1.0, v23
	v_rcp_f32_e32 v15, v28
	s_nop 0
	v_mul_f32_e32 v12, v12, v15
	v_mul_f32_e32 v15, v20, v12
	v_rcp_f32_e32 v12, v23
	s_nop 0
	v_mul_f32_e32 v12, v13, v12
	v_mul_f32_e32 v13, v21, v12
	v_mul_f32_e32 v12, 0xbfb8aa3b, v18
	v_exp_f32_e32 v20, v12
	v_med3_f32 v11, v11, s75, v233
	v_med3_f32 v14, v14, s75, v233
	v_mov_b32_e32 v12, v203
	v_cvt_pk_fp8_f32 v12, v11, v14
	v_add_f32_e32 v11, 1.0, v20
	v_med3_f32 v15, v15, s75, v233
	v_med3_f32 v13, v13, s75, v233
	v_cvt_pk_fp8_f32 v12, v15, v13 op_sel:[0,0,1]
	v_mul_f32_e32 v21, 0xbfb8aa3b, v19
	v_exp_f32_e32 v21, v21
	s_nop 0
	v_add_f32_e32 v14, 1.0, v21
	v_pk_mul_f32 v[16:17], v[116:117], s[28:29] op_sel_hi:[1,0]
	v_rcp_f32_e32 v11, v11
	s_nop 0
	v_mul_f32_e32 v11, v18, v11
	v_mul_f32_e32 v18, 0xbfb8aa3b, v16
	v_exp_f32_e32 v18, v18
	s_nop 0
	v_add_f32_e32 v18, 1.0, v18
	v_rcp_f32_e32 v13, v14
	s_nop 0
	v_mul_f32_e32 v13, v19, v13
	v_mul_f32_e32 v19, 0xbfb8aa3b, v17
	v_exp_f32_e32 v19, v19
	s_nop 0
	v_add_f32_e32 v19, 1.0, v19
	v_rcp_f32_e32 v14, v18
	s_nop 0
	v_mul_f32_e32 v14, v16, v14
	v_pk_mul_f32 v[26:27], v[82:83], s[30:31] op_sel_hi:[1,0]
	v_mul_f32_e32 v11, v26, v11
	v_mul_f32_e32 v13, v27, v13
	v_med3_f32 v11, v11, s75, v233
	v_med3_f32 v16, v13, s75, v233
	v_mov_b32_e32 v13, v203
	v_cvt_pk_fp8_f32 v13, v11, v16
	v_pk_mul_f32 v[24:25], v[84:85], s[30:31] op_sel_hi:[1,0]
	v_rcp_f32_e32 v15, v19
	s_nop 0
	v_mul_f32_e32 v15, v17, v15
	ds_read_b128 v[2:5], v9 offset:1024
	v_mul_f32_e32 v14, v24, v14
	v_mul_f32_e32 v11, v25, v15
	v_med3_f32 v14, v14, s75, v233
	v_med3_f32 v11, v11, s75, v233
	v_cvt_pk_fp8_f32 v13, v14, v11 op_sel:[0,0,1]
	v_add_u32_e32 v11, 0x4000, v10
	s_waitcnt lgkmcnt(0)
	global_store_dwordx4 v11, v[2:5], s[16:17] nt
	ds_write_b64 v8, v[6:7]
	ds_write_b64 v8, v[12:13] offset:512
	v_pk_mul_f32 v[12:13], v[110:111], s[28:29] op_sel_hi:[1,0]
	v_pk_mul_f32 v[6:7], v[112:113], s[28:29] op_sel_hi:[1,0]
	v_mul_f32_e32 v11, 0xbfb8aa3b, v12
	v_exp_f32_e32 v11, v11
	v_mul_f32_e32 v30, 0xbfb8aa3b, v13
	v_exp_f32_e32 v30, v30
	v_pk_mul_f32 v[20:21], v[78:79], s[30:31] op_sel_hi:[1,0]
	v_add_f32_e32 v11, 1.0, v11
	v_pk_mul_f32 v[18:19], v[80:81], s[30:31] op_sel_hi:[1,0]
	v_pk_mul_f32 v[16:17], v[106:107], s[28:29] op_sel_hi:[1,0]
	v_pk_mul_f32 v[14:15], v[108:109], s[28:29] op_sel_hi:[1,0]
	v_add_f32_e32 v28, 1.0, v30
	v_rcp_f32_e32 v11, v11
	s_nop 0
	v_mul_f32_e32 v11, v12, v11
	v_mul_f32_e32 v26, 0xbfb8aa3b, v6
	v_exp_f32_e32 v26, v26
	v_mul_f32_e32 v11, v20, v11
	v_add_f32_e32 v26, 1.0, v26
	v_rcp_f32_e32 v12, v28
	s_nop 0
	v_mul_f32_e32 v12, v13, v12
	v_mul_f32_e32 v12, v21, v12
	v_mul_f32_e32 v21, 0xbfb8aa3b, v7
	v_exp_f32_e32 v21, v21
	s_nop 0
	v_add_f32_e32 v21, 1.0, v21
	v_rcp_f32_e32 v13, v26
	s_nop 0
	v_mul_f32_e32 v6, v6, v13
	v_mul_f32_e32 v13, v18, v6
	v_rcp_f32_e32 v6, v21
	s_nop 0
	v_mul_f32_e32 v6, v7, v6
	v_mul_f32_e32 v7, v19, v6
	v_mul_f32_e32 v6, 0xbfb8aa3b, v16
	v_exp_f32_e32 v18, v6
	v_med3_f32 v11, v11, s75, v233
	v_med3_f32 v12, v12, s75, v233
	v_mov_b32_e32 v6, v203
	v_cvt_pk_fp8_f32 v6, v11, v12
	v_add_f32_e32 v11, 1.0, v18
	v_med3_f32 v13, v13, s75, v233
	v_med3_f32 v7, v7, s75, v233
	v_cvt_pk_fp8_f32 v6, v13, v7 op_sel:[0,0,1]
	v_mul_f32_e32 v19, 0xbfb8aa3b, v17
	v_exp_f32_e32 v19, v19
	s_nop 0
	v_add_f32_e32 v12, 1.0, v19
	v_rcp_f32_e32 v7, v11
	s_nop 0
	v_mul_f32_e32 v7, v16, v7
	v_mul_f32_e32 v16, 0xbfb8aa3b, v14
	v_exp_f32_e32 v16, v16
	s_nop 0
	v_add_f32_e32 v16, 1.0, v16
	v_rcp_f32_e32 v11, v12
	s_nop 0
	v_mul_f32_e32 v11, v17, v11
	v_mul_f32_e32 v17, 0xbfb8aa3b, v15
	v_exp_f32_e32 v17, v17
	s_nop 0
	v_add_f32_e32 v17, 1.0, v17
	v_rcp_f32_e32 v12, v16
	s_nop 0
	v_mul_f32_e32 v12, v14, v12
	v_pk_mul_f32 v[24:25], v[74:75], s[30:31] op_sel_hi:[1,0]
	v_mul_f32_e32 v7, v24, v7
	v_mul_f32_e32 v11, v25, v11
	v_med3_f32 v14, v7, s75, v233
	v_med3_f32 v11, v11, s75, v233
	v_mov_b32_e32 v7, v203
	v_cvt_pk_fp8_f32 v7, v14, v11
	v_pk_mul_f32 v[22:23], v[76:77], s[30:31] op_sel_hi:[1,0]
	v_rcp_f32_e32 v13, v17
	s_nop 0
	v_mul_f32_e32 v13, v15, v13
	v_mul_f32_e32 v12, v22, v12
	v_mul_f32_e32 v11, v23, v13
	v_med3_f32 v12, v12, s75, v233
	v_med3_f32 v11, v11, s75, v233
	v_pk_mul_f32 v[14:15], v[102:103], s[28:29] op_sel_hi:[1,0]
	v_cvt_pk_fp8_f32 v7, v12, v11 op_sel:[0,0,1]
	v_mul_f32_e32 v11, 0xbfb8aa3b, v14
	v_exp_f32_e32 v11, v11
	v_mul_f32_e32 v32, 0xbfb8aa3b, v15
	v_exp_f32_e32 v32, v32
	v_pk_mul_f32 v[12:13], v[104:105], s[28:29] op_sel_hi:[1,0]
	v_add_f32_e32 v11, 1.0, v11
	v_pk_mul_f32 v[22:23], v[70:71], s[30:31] op_sel_hi:[1,0]
	v_pk_mul_f32 v[20:21], v[72:73], s[30:31] op_sel_hi:[1,0]
	v_pk_mul_f32 v[18:19], v[98:99], s[28:29] op_sel_hi:[1,0]
	v_add_f32_e32 v30, 1.0, v32
	v_rcp_f32_e32 v11, v11
	s_nop 0
	v_mul_f32_e32 v11, v14, v11
	v_mul_f32_e32 v28, 0xbfb8aa3b, v12
	v_exp_f32_e32 v28, v28
	v_mul_f32_e32 v11, v22, v11
	v_add_f32_e32 v28, 1.0, v28
	v_rcp_f32_e32 v14, v30
	s_nop 0
	v_mul_f32_e32 v14, v15, v14
	v_mul_f32_e32 v14, v23, v14
	v_mul_f32_e32 v23, 0xbfb8aa3b, v13
	v_exp_f32_e32 v23, v23
	s_nop 0
	v_add_f32_e32 v23, 1.0, v23
	v_rcp_f32_e32 v15, v28
	s_nop 0
	v_mul_f32_e32 v12, v12, v15
	v_mul_f32_e32 v15, v20, v12
	v_rcp_f32_e32 v12, v23
	s_nop 0
	v_mul_f32_e32 v12, v13, v12
	v_mul_f32_e32 v13, v21, v12
	v_mul_f32_e32 v12, 0xbfb8aa3b, v18
	v_exp_f32_e32 v20, v12
	v_med3_f32 v11, v11, s75, v233
	v_med3_f32 v14, v14, s75, v233
	v_mov_b32_e32 v12, v203
	v_cvt_pk_fp8_f32 v12, v11, v14
	v_add_f32_e32 v11, 1.0, v20
	v_med3_f32 v15, v15, s75, v233
	v_med3_f32 v13, v13, s75, v233
	v_cvt_pk_fp8_f32 v12, v15, v13 op_sel:[0,0,1]
	v_mul_f32_e32 v21, 0xbfb8aa3b, v19
	v_exp_f32_e32 v21, v21
	s_nop 0
	v_add_f32_e32 v14, 1.0, v21
	v_pk_mul_f32 v[16:17], v[100:101], s[28:29] op_sel_hi:[1,0]
	v_rcp_f32_e32 v11, v11
	s_nop 0
	v_mul_f32_e32 v11, v18, v11
	v_mul_f32_e32 v18, 0xbfb8aa3b, v16
	v_exp_f32_e32 v18, v18
	s_nop 0
	v_add_f32_e32 v18, 1.0, v18
	v_rcp_f32_e32 v13, v14
	s_nop 0
	v_mul_f32_e32 v13, v19, v13
	v_mul_f32_e32 v19, 0xbfb8aa3b, v17
	v_exp_f32_e32 v19, v19
	s_nop 0
	v_add_f32_e32 v19, 1.0, v19
	v_rcp_f32_e32 v14, v18
	s_nop 0
	v_mul_f32_e32 v14, v16, v14
	v_pk_mul_f32 v[26:27], v[66:67], s[30:31] op_sel_hi:[1,0]
	v_mul_f32_e32 v11, v26, v11
	v_mul_f32_e32 v13, v27, v13
	v_med3_f32 v11, v11, s75, v233
	v_med3_f32 v16, v13, s75, v233
	v_mov_b32_e32 v13, v203
	v_cvt_pk_fp8_f32 v13, v11, v16
	v_pk_mul_f32 v[24:25], v[68:69], s[30:31] op_sel_hi:[1,0]
	v_rcp_f32_e32 v15, v19
	s_nop 0
	v_mul_f32_e32 v15, v17, v15
	ds_read_b128 v[2:5], v9
	v_mul_f32_e32 v14, v24, v14
	v_mul_f32_e32 v11, v25, v15
	v_med3_f32 v14, v14, s75, v233
	v_med3_f32 v11, v11, s75, v233
	v_cvt_pk_fp8_f32 v13, v14, v11 op_sel:[0,0,1]
	v_add_u32_e32 v11, 0x10000, v10
	s_waitcnt lgkmcnt(0)
	global_store_dwordx4 v11, v[2:5], s[16:17] nt
	ds_write_b64 v8, v[6:7] offset:1024
	ds_write_b64 v8, v[12:13] offset:1536
	ds_read_b128 v[2:5], v9 offset:1024
	v_add_u32_e32 v6, 0x14000, v10
	s_andn2_b64 vcc, exec, s[42:43]
	s_waitcnt lgkmcnt(0)
	global_store_dwordx4 v6, v[2:5], s[16:17] nt
	s_cbranch_vccnz .LBB0_1856
	s_andn2_b64 vcc, exec, s[20:21]
	s_cbranch_vccnz .LBB0_1823
	s_barrier
	s_branch .LBB0_1823

.LBB0_1974:
	v_pk_mul_f32 v[4:5], v[186:187], v[0:1] op_sel_hi:[1,0]
	v_pk_mul_f32 v[6:7], v[184:185], v[0:1] op_sel_hi:[1,0]
	v_pk_mul_f32 v[10:11], v[180:181], v[0:1] op_sel_hi:[1,0]
	v_med3_f32 v3, v6, s74, v250
	v_med3_f32 v6, v7, s74, v250
	v_med3_f32 v7, v4, s74, v250
	v_mov_b32_e32 v4, v207
	v_med3_f32 v18, v5, s74, v250
	v_cvt_pk_fp8_f32 v4, v3, v6
	v_med3_f32 v3, v10, s74, v250
	v_med3_f32 v6, v11, s74, v250
	v_mov_b32_e32 v5, v207
	v_cvt_pk_fp8_f32 v5, v3, v6
	v_pk_mul_f32 v[8:9], v[182:183], v[0:1] op_sel_hi:[1,0]
	v_pk_mul_f32 v[14:15], v[192:193], v[0:1] op_sel_hi:[1,0]
	v_med3_f32 v3, v8, s74, v250
	v_med3_f32 v6, v9, s74, v250
	v_pk_mul_f32 v[12:13], v[194:195], v[0:1] op_sel_hi:[1,0]
	v_pk_mul_f32 v[16:17], v[190:191], v[0:1] op_sel_hi:[1,0]
	v_pk_mul_f32 v[0:1], v[188:189], v[0:1] op_sel_hi:[1,0]
	v_cvt_pk_fp8_f32 v4, v7, v18 op_sel:[0,0,1]
	v_cvt_pk_fp8_f32 v5, v3, v6 op_sel:[0,0,1]
	v_med3_f32 v3, v14, s74, v250
	v_med3_f32 v7, v15, s74, v250
	v_mov_b32_e32 v6, v207
	v_cvt_pk_fp8_f32 v6, v3, v7
	v_med3_f32 v0, v0, s74, v250
	v_med3_f32 v1, v1, s74, v250
	v_mov_b32_e32 v7, v207
	v_cvt_pk_fp8_f32 v7, v0, v1
	v_med3_f32 v8, v12, s74, v250
	v_med3_f32 v9, v13, s74, v250
	v_med3_f32 v0, v16, s74, v250
	v_med3_f32 v1, v17, s74, v250
	v_cvt_pk_fp8_f32 v6, v8, v9 op_sel:[0,0,1]
	v_cvt_pk_fp8_f32 v7, v0, v1 op_sel:[0,0,1]
	v_add_u32_e32 v0, v232, v236
	v_ashrrev_i32_e32 v1, 31, v0
	v_lshlrev_b64 v[8:9], 11, v[0:1]
	ds_write_b128 v251, v[4:7]
	ds_read_b128 v[4:7], v252
	s_lshl_b32 s40, s40, 8
	v_lshl_add_u64 v[8:9], s[16:17], 0, v[8:9]
	s_ashr_i32 s41, s40, 31
	v_lshl_add_u64 v[8:9], v[8:9], 0, s[40:41]
	v_lshl_add_u64 v[8:9], v[8:9], 0, s[12:13]
	v_cndmask_b32_e64 v1, 0, 1, s[46:47]
	v_lshl_add_u64 v[8:9], v[8:9], 0, v[214:215]
	v_cmp_ne_u32_e64 s[2:3], 1, v1
	s_andn2_b64 vcc, exec, s[46:47]
	s_waitcnt lgkmcnt(0)
	global_store_dwordx4 v[8:9], v[4:7], off nt
	s_cbranch_vccnz .LBB0_1978
	v_or_b32_e32 v1, 16, v234
	v_cmp_lt_i32_e32 vcc, v1, v233
	s_waitcnt vmcnt(6)
	v_mul_f32_e32 v2, 0.5, v25
	v_cndmask_b32_e32 v2, 0, v2, vcc
.LBB0_1978:
	s_nop 0
	v_pk_mul_f32 v[6:7], v[168:169], v[2:3] op_sel_hi:[1,0]
	v_pk_mul_f32 v[4:5], v[170:171], v[2:3] op_sel_hi:[1,0]
	v_pk_mul_f32 v[8:9], v[166:167], v[2:3] op_sel_hi:[1,0]
	v_pk_mul_f32 v[10:11], v[164:165], v[2:3] op_sel_hi:[1,0]
	v_pk_mul_f32 v[12:13], v[178:179], v[2:3] op_sel_hi:[1,0]
	v_pk_mul_f32 v[14:15], v[176:177], v[2:3] op_sel_hi:[1,0]
	v_pk_mul_f32 v[16:17], v[174:175], v[2:3] op_sel_hi:[1,0]
	v_pk_mul_f32 v[18:19], v[172:173], v[2:3] op_sel_hi:[1,0]
	v_med3_f32 v1, v6, s74, v250
	v_med3_f32 v3, v7, s74, v250
	v_mov_b32_e32 v2, v207
	v_cvt_pk_fp8_f32 v2, v1, v3
	v_med3_f32 v1, v10, s74, v250
	v_med3_f32 v6, v11, s74, v250
	v_mov_b32_e32 v3, v207
	v_cvt_pk_fp8_f32 v3, v1, v6
	v_med3_f32 v4, v4, s74, v250
	v_med3_f32 v5, v5, s74, v250
	v_cvt_pk_fp8_f32 v2, v4, v5 op_sel:[0,0,1]
	v_med3_f32 v1, v8, s74, v250
	v_med3_f32 v4, v9, s74, v250
	v_cvt_pk_fp8_f32 v3, v1, v4 op_sel:[0,0,1]
	v_med3_f32 v1, v14, s74, v250
	v_med3_f32 v5, v15, s74, v250
	v_mov_b32_e32 v4, v207
	v_cvt_pk_fp8_f32 v4, v1, v5
	v_med3_f32 v1, v18, s74, v250
	v_med3_f32 v8, v19, s74, v250
	v_mov_b32_e32 v5, v207
	v_cvt_pk_fp8_f32 v5, v1, v8
	v_med3_f32 v6, v12, s74, v250
	v_med3_f32 v7, v13, s74, v250
	v_cvt_pk_fp8_f32 v4, v6, v7 op_sel:[0,0,1]
	v_med3_f32 v1, v16, s74, v250
	v_med3_f32 v6, v17, s74, v250
	v_cvt_pk_fp8_f32 v5, v1, v6 op_sel:[0,0,1]
	v_or_b32_e32 v1, 16, v236
	v_add_u32_e32 v6, v1, v232
	v_ashrrev_i32_e32 v7, 31, v6
	ds_write_b128 v251, v[2:5] offset:1024
	ds_read_b128 v[2:5], v252 offset:1024
	v_lshlrev_b64 v[6:7], 11, v[6:7]
	v_lshl_add_u64 v[6:7], s[16:17], 0, v[6:7]
	v_lshl_add_u64 v[6:7], v[6:7], 0, s[40:41]
	v_lshl_add_u64 v[6:7], v[6:7], 0, s[12:13]
	v_lshl_add_u64 v[6:7], v[6:7], 0, v[214:215]
	s_waitcnt lgkmcnt(0)
	global_store_dwordx4 v[6:7], v[2:5], off nt
	s_and_b64 vcc, exec, s[2:3]
	s_nop 0
	v_mov_b32_e32 v2, 0.5
	v_mov_b32_e32 v4, 0.5
	s_cbranch_vccnz .LBB0_1982
	v_or_b32_e32 v1, 32, v234
	v_cmp_lt_i32_e32 vcc, v1, v233
	s_waitcnt vmcnt(5)
	v_mul_f32_e32 v4, 0.5, v26
	v_cndmask_b32_e32 v4, 0, v4, vcc
.LBB0_1982:
	v_pk_mul_f32 v[8:9], v[152:153], v[4:5] op_sel_hi:[1,0]
	v_pk_mul_f32 v[6:7], v[154:155], v[4:5] op_sel_hi:[1,0]
	v_pk_mul_f32 v[10:11], v[150:151], v[4:5] op_sel_hi:[1,0]
	v_pk_mul_f32 v[12:13], v[148:149], v[4:5] op_sel_hi:[1,0]
	v_pk_mul_f32 v[14:15], v[162:163], v[4:5] op_sel_hi:[1,0]
	v_pk_mul_f32 v[16:17], v[160:161], v[4:5] op_sel_hi:[1,0]
	v_pk_mul_f32 v[18:19], v[158:159], v[4:5] op_sel_hi:[1,0]
	v_pk_mul_f32 v[20:21], v[156:157], v[4:5] op_sel_hi:[1,0]
	v_med3_f32 v1, v8, s74, v250
	v_med3_f32 v3, v9, s74, v250
	v_mov_b32_e32 v4, v207
	v_cvt_pk_fp8_f32 v4, v1, v3
	v_med3_f32 v1, v12, s74, v250
	v_med3_f32 v3, v13, s74, v250
	v_mov_b32_e32 v5, v207
	v_cvt_pk_fp8_f32 v5, v1, v3
	v_med3_f32 v6, v6, s74, v250
	v_med3_f32 v7, v7, s74, v250
	v_med3_f32 v1, v10, s74, v250
	v_med3_f32 v3, v11, s74, v250
	v_cvt_pk_fp8_f32 v4, v6, v7 op_sel:[0,0,1]
	v_cvt_pk_fp8_f32 v5, v1, v3 op_sel:[0,0,1]
	v_med3_f32 v1, v16, s74, v250
	v_med3_f32 v3, v17, s74, v250
	v_mov_b32_e32 v6, v207
	v_cvt_pk_fp8_f32 v6, v1, v3
	v_med3_f32 v1, v20, s74, v250
	v_med3_f32 v3, v21, s74, v250
	v_mov_b32_e32 v7, v207
	v_cvt_pk_fp8_f32 v7, v1, v3
	v_med3_f32 v8, v14, s74, v250
	v_med3_f32 v9, v15, s74, v250
	v_med3_f32 v1, v18, s74, v250
	v_med3_f32 v3, v19, s74, v250
	v_cvt_pk_fp8_f32 v6, v8, v9 op_sel:[0,0,1]
	v_cvt_pk_fp8_f32 v7, v1, v3 op_sel:[0,0,1]
	v_add_u32_e32 v8, v239, v232
	v_ashrrev_i32_e32 v9, 31, v8
	v_lshlrev_b64 v[8:9], 11, v[8:9]
	ds_write_b128 v251, v[4:7]
	ds_read_b128 v[4:7], v252
	v_lshl_add_u64 v[8:9], s[16:17], 0, v[8:9]
	v_lshl_add_u64 v[8:9], v[8:9], 0, s[40:41]
	v_lshl_add_u64 v[8:9], v[8:9], 0, s[12:13]
	v_lshl_add_u64 v[8:9], v[8:9], 0, v[214:215]
	s_and_b64 vcc, exec, s[2:3]
	s_waitcnt lgkmcnt(0)
	global_store_dwordx4 v[8:9], v[4:7], off nt
	s_cbranch_vccnz .LBB0_1986
	v_or_b32_e32 v1, 48, v234
	v_cmp_lt_i32_e32 vcc, v1, v233
	s_waitcnt vmcnt(4)
	v_mul_f32_e32 v2, 0.5, v27
	v_cndmask_b32_e32 v2, 0, v2, vcc
.LBB0_1986:
	s_nop 0
	v_pk_mul_f32 v[6:7], v[120:121], v[2:3] op_sel_hi:[1,0]
	v_pk_mul_f32 v[4:5], v[122:123], v[2:3] op_sel_hi:[1,0]
	v_pk_mul_f32 v[8:9], v[118:119], v[2:3] op_sel_hi:[1,0]
	v_pk_mul_f32 v[10:11], v[116:117], v[2:3] op_sel_hi:[1,0]
	v_pk_mul_f32 v[12:13], v[130:131], v[2:3] op_sel_hi:[1,0]
	v_pk_mul_f32 v[14:15], v[128:129], v[2:3] op_sel_hi:[1,0]
	v_pk_mul_f32 v[16:17], v[126:127], v[2:3] op_sel_hi:[1,0]
	v_pk_mul_f32 v[18:19], v[124:125], v[2:3] op_sel_hi:[1,0]
	v_med3_f32 v1, v6, s74, v250
	v_med3_f32 v3, v7, s74, v250
	v_mov_b32_e32 v2, v207
	v_cvt_pk_fp8_f32 v2, v1, v3
	v_med3_f32 v1, v10, s74, v250
	v_med3_f32 v6, v11, s74, v250
	v_mov_b32_e32 v3, v207
	v_cvt_pk_fp8_f32 v3, v1, v6
	v_med3_f32 v4, v4, s74, v250
	v_med3_f32 v5, v5, s74, v250
	v_cvt_pk_fp8_f32 v2, v4, v5 op_sel:[0,0,1]
	v_med3_f32 v1, v8, s74, v250
	v_med3_f32 v4, v9, s74, v250
	v_cvt_pk_fp8_f32 v3, v1, v4 op_sel:[0,0,1]
	v_med3_f32 v1, v14, s74, v250
	v_med3_f32 v5, v15, s74, v250
	v_mov_b32_e32 v4, v207
	v_cvt_pk_fp8_f32 v4, v1, v5
	v_med3_f32 v1, v18, s74, v250
	v_med3_f32 v8, v19, s74, v250
	v_mov_b32_e32 v5, v207
	v_cvt_pk_fp8_f32 v5, v1, v8
	v_med3_f32 v6, v12, s74, v250
	v_med3_f32 v7, v13, s74, v250
	v_cvt_pk_fp8_f32 v4, v6, v7 op_sel:[0,0,1]
	v_med3_f32 v1, v16, s74, v250
	v_med3_f32 v6, v17, s74, v250
	v_cvt_pk_fp8_f32 v5, v1, v6 op_sel:[0,0,1]
	v_add_u32_e32 v6, v241, v232
	v_ashrrev_i32_e32 v7, 31, v6
	v_lshlrev_b64 v[6:7], 11, v[6:7]
	ds_write_b128 v251, v[2:5] offset:1024
	ds_read_b128 v[2:5], v252 offset:1024
	v_lshl_add_u64 v[6:7], s[16:17], 0, v[6:7]
	v_lshl_add_u64 v[6:7], v[6:7], 0, s[40:41]
	v_lshl_add_u64 v[6:7], v[6:7], 0, s[12:13]
	v_lshl_add_u64 v[6:7], v[6:7], 0, v[214:215]
	s_waitcnt lgkmcnt(0)
	global_store_dwordx4 v[6:7], v[2:5], off nt
	s_and_b64 vcc, exec, s[2:3]
	s_nop 0
	v_mov_b32_e32 v2, 0.5
	v_mov_b32_e32 v4, 0.5
	s_cbranch_vccnz .LBB0_1990
	v_add_u32_e32 v1, 0x80, v234
	v_cmp_lt_i32_e32 vcc, v1, v233
	s_waitcnt vmcnt(3)
	v_mul_f32_e32 v4, 0.5, v28
	v_cndmask_b32_e32 v4, 0, v4, vcc
.LBB0_1990:
	v_pk_mul_f32 v[8:9], v[136:137], v[4:5] op_sel_hi:[1,0]
	v_pk_mul_f32 v[6:7], v[138:139], v[4:5] op_sel_hi:[1,0]
	v_pk_mul_f32 v[10:11], v[134:135], v[4:5] op_sel_hi:[1,0]
	v_pk_mul_f32 v[12:13], v[132:133], v[4:5] op_sel_hi:[1,0]
	v_pk_mul_f32 v[14:15], v[146:147], v[4:5] op_sel_hi:[1,0]
	v_pk_mul_f32 v[16:17], v[144:145], v[4:5] op_sel_hi:[1,0]
	v_pk_mul_f32 v[18:19], v[142:143], v[4:5] op_sel_hi:[1,0]
	v_pk_mul_f32 v[20:21], v[140:141], v[4:5] op_sel_hi:[1,0]
	v_med3_f32 v1, v8, s74, v250
	v_med3_f32 v3, v9, s74, v250
	v_mov_b32_e32 v4, v207
	v_cvt_pk_fp8_f32 v4, v1, v3
	v_med3_f32 v1, v12, s74, v250
	v_med3_f32 v3, v13, s74, v250
	v_mov_b32_e32 v5, v207
	v_cvt_pk_fp8_f32 v5, v1, v3
	v_med3_f32 v6, v6, s74, v250
	v_med3_f32 v7, v7, s74, v250
	v_med3_f32 v1, v10, s74, v250
	v_med3_f32 v3, v11, s74, v250
	v_cvt_pk_fp8_f32 v4, v6, v7 op_sel:[0,0,1]
	v_cvt_pk_fp8_f32 v5, v1, v3 op_sel:[0,0,1]
	v_med3_f32 v1, v16, s74, v250
	v_med3_f32 v3, v17, s74, v250
	v_mov_b32_e32 v6, v207
	v_cvt_pk_fp8_f32 v6, v1, v3
	v_med3_f32 v1, v20, s74, v250
	v_med3_f32 v3, v21, s74, v250
	v_mov_b32_e32 v7, v207
	v_cvt_pk_fp8_f32 v7, v1, v3
	v_med3_f32 v8, v14, s74, v250
	v_med3_f32 v9, v15, s74, v250
	v_med3_f32 v1, v18, s74, v250
	v_med3_f32 v3, v19, s74, v250
	v_cvt_pk_fp8_f32 v6, v8, v9 op_sel:[0,0,1]
	v_cvt_pk_fp8_f32 v7, v1, v3 op_sel:[0,0,1]
	v_add_u32_e32 v8, 0x80, v0
	v_ashrrev_i32_e32 v9, 31, v8
	v_lshlrev_b64 v[8:9], 11, v[8:9]
	ds_write_b128 v251, v[4:7]
	ds_read_b128 v[4:7], v252
	v_lshl_add_u64 v[8:9], s[16:17], 0, v[8:9]
	v_lshl_add_u64 v[8:9], v[8:9], 0, s[40:41]
	v_lshl_add_u64 v[8:9], v[8:9], 0, s[12:13]
	v_lshl_add_u64 v[8:9], v[8:9], 0, v[214:215]
	s_and_b64 vcc, exec, s[2:3]
	s_waitcnt lgkmcnt(0)
	global_store_dwordx4 v[8:9], v[4:7], off nt
	s_cbranch_vccnz .LBB0_1994
	v_add_u32_e32 v1, 0x90, v234
	v_cmp_lt_i32_e32 vcc, v1, v233
	s_waitcnt vmcnt(2)
	v_mul_f32_e32 v2, 0.5, v29
	v_cndmask_b32_e32 v2, 0, v2, vcc
.LBB0_1994:
	s_nop 0
	v_pk_mul_f32 v[6:7], v[104:105], v[2:3] op_sel_hi:[1,0]
	v_pk_mul_f32 v[4:5], v[106:107], v[2:3] op_sel_hi:[1,0]
	v_pk_mul_f32 v[8:9], v[102:103], v[2:3] op_sel_hi:[1,0]
	v_pk_mul_f32 v[10:11], v[100:101], v[2:3] op_sel_hi:[1,0]
	v_pk_mul_f32 v[12:13], v[114:115], v[2:3] op_sel_hi:[1,0]
	v_pk_mul_f32 v[14:15], v[112:113], v[2:3] op_sel_hi:[1,0]
	v_pk_mul_f32 v[16:17], v[110:111], v[2:3] op_sel_hi:[1,0]
	v_pk_mul_f32 v[18:19], v[108:109], v[2:3] op_sel_hi:[1,0]
	v_med3_f32 v1, v6, s74, v250
	v_med3_f32 v3, v7, s74, v250
	v_mov_b32_e32 v2, v207
	v_cvt_pk_fp8_f32 v2, v1, v3
	v_med3_f32 v1, v10, s74, v250
	v_med3_f32 v6, v11, s74, v250
	v_mov_b32_e32 v3, v207
	v_cvt_pk_fp8_f32 v3, v1, v6
	v_med3_f32 v4, v4, s74, v250
	v_med3_f32 v5, v5, s74, v250
	v_cvt_pk_fp8_f32 v2, v4, v5 op_sel:[0,0,1]
	v_med3_f32 v1, v8, s74, v250
	v_med3_f32 v4, v9, s74, v250
	v_cvt_pk_fp8_f32 v3, v1, v4 op_sel:[0,0,1]
	v_med3_f32 v1, v14, s74, v250
	v_med3_f32 v5, v15, s74, v250
	v_mov_b32_e32 v4, v207
	v_cvt_pk_fp8_f32 v4, v1, v5
	v_med3_f32 v1, v18, s74, v250
	v_med3_f32 v8, v19, s74, v250
	v_mov_b32_e32 v5, v207
	v_cvt_pk_fp8_f32 v5, v1, v8
	v_med3_f32 v6, v12, s74, v250
	v_med3_f32 v7, v13, s74, v250
	v_cvt_pk_fp8_f32 v4, v6, v7 op_sel:[0,0,1]
	v_med3_f32 v1, v16, s74, v250
	v_med3_f32 v6, v17, s74, v250
	v_cvt_pk_fp8_f32 v5, v1, v6 op_sel:[0,0,1]
	v_add_u32_e32 v6, 0x90, v0
	v_ashrrev_i32_e32 v7, 31, v6
	v_lshlrev_b64 v[6:7], 11, v[6:7]
	ds_write_b128 v251, v[2:5] offset:1024
	ds_read_b128 v[2:5], v252 offset:1024
	v_lshl_add_u64 v[6:7], s[16:17], 0, v[6:7]
	v_lshl_add_u64 v[6:7], v[6:7], 0, s[40:41]
	v_lshl_add_u64 v[6:7], v[6:7], 0, s[12:13]
	v_lshl_add_u64 v[6:7], v[6:7], 0, v[214:215]
	s_waitcnt lgkmcnt(0)
	global_store_dwordx4 v[6:7], v[2:5], off nt
	s_and_b64 vcc, exec, s[2:3]
	s_nop 0
	v_mov_b32_e32 v2, 0.5
	v_mov_b32_e32 v4, 0.5
	s_cbranch_vccnz .LBB0_1998
	v_cmp_lt_i32_e32 vcc, v244, v233
	s_waitcnt vmcnt(1)
	v_mul_f32_e32 v4, 0.5, v30
	v_cndmask_b32_e32 v4, 0, v4, vcc
.LBB0_1998:
	v_pk_mul_f32 v[8:9], v[88:89], v[4:5] op_sel_hi:[1,0]
	v_pk_mul_f32 v[6:7], v[90:91], v[4:5] op_sel_hi:[1,0]
	v_pk_mul_f32 v[10:11], v[86:87], v[4:5] op_sel_hi:[1,0]
	v_pk_mul_f32 v[12:13], v[84:85], v[4:5] op_sel_hi:[1,0]
	v_pk_mul_f32 v[14:15], v[98:99], v[4:5] op_sel_hi:[1,0]
	v_pk_mul_f32 v[16:17], v[96:97], v[4:5] op_sel_hi:[1,0]
	v_pk_mul_f32 v[18:19], v[94:95], v[4:5] op_sel_hi:[1,0]
	v_pk_mul_f32 v[20:21], v[92:93], v[4:5] op_sel_hi:[1,0]
	v_med3_f32 v1, v8, s74, v250
	v_med3_f32 v3, v9, s74, v250
	v_mov_b32_e32 v4, v207
	v_cvt_pk_fp8_f32 v4, v1, v3
	v_med3_f32 v1, v12, s74, v250
	v_med3_f32 v3, v13, s74, v250
	v_mov_b32_e32 v5, v207
	v_cvt_pk_fp8_f32 v5, v1, v3
	v_med3_f32 v6, v6, s74, v250
	v_med3_f32 v7, v7, s74, v250
	v_med3_f32 v1, v10, s74, v250
	v_med3_f32 v3, v11, s74, v250
	v_cvt_pk_fp8_f32 v4, v6, v7 op_sel:[0,0,1]
	v_cvt_pk_fp8_f32 v5, v1, v3 op_sel:[0,0,1]
	v_med3_f32 v1, v16, s74, v250
	v_med3_f32 v3, v17, s74, v250
	v_mov_b32_e32 v6, v207
	v_cvt_pk_fp8_f32 v6, v1, v3
	v_med3_f32 v1, v20, s74, v250
	v_med3_f32 v3, v21, s74, v250
	v_mov_b32_e32 v7, v207
	v_cvt_pk_fp8_f32 v7, v1, v3
	v_med3_f32 v8, v14, s74, v250
	v_med3_f32 v9, v15, s74, v250
	v_med3_f32 v1, v18, s74, v250
	v_med3_f32 v3, v19, s74, v250
	v_cvt_pk_fp8_f32 v6, v8, v9 op_sel:[0,0,1]
	v_cvt_pk_fp8_f32 v7, v1, v3 op_sel:[0,0,1]
	v_add_u32_e32 v8, 0xa0, v0
	v_ashrrev_i32_e32 v9, 31, v8
	v_lshlrev_b64 v[8:9], 11, v[8:9]
	ds_write_b128 v251, v[4:7]
	ds_read_b128 v[4:7], v252
	v_lshl_add_u64 v[8:9], s[16:17], 0, v[8:9]
	v_lshl_add_u64 v[8:9], v[8:9], 0, s[40:41]
	v_lshl_add_u64 v[8:9], v[8:9], 0, s[12:13]
	v_lshl_add_u64 v[8:9], v[8:9], 0, v[214:215]
	s_and_b64 vcc, exec, s[2:3]
	s_waitcnt lgkmcnt(0)
	global_store_dwordx4 v[8:9], v[4:7], off nt
	s_cbranch_vccnz .LBB0_2002
	v_cmp_lt_i32_e32 vcc, v245, v233
	s_waitcnt vmcnt(0)
	v_mul_f32_e32 v2, 0.5, v31
	v_cndmask_b32_e32 v2, 0, v2, vcc
.LBB0_2002:
	s_nop 0
	v_pk_mul_f32 v[6:7], v[76:77], v[2:3] op_sel_hi:[1,0]
	v_pk_mul_f32 v[4:5], v[78:79], v[2:3] op_sel_hi:[1,0]
	v_pk_mul_f32 v[8:9], v[74:75], v[2:3] op_sel_hi:[1,0]
	v_pk_mul_f32 v[10:11], v[72:73], v[2:3] op_sel_hi:[1,0]
	v_pk_mul_f32 v[12:13], v[82:83], v[2:3] op_sel_hi:[1,0]
	v_pk_mul_f32 v[14:15], v[80:81], v[2:3] op_sel_hi:[1,0]
	v_pk_mul_f32 v[16:17], v[70:71], v[2:3] op_sel_hi:[1,0]
	v_pk_mul_f32 v[18:19], v[68:69], v[2:3] op_sel_hi:[1,0]
	v_med3_f32 v1, v6, s74, v250
	v_med3_f32 v3, v7, s74, v250
	v_mov_b32_e32 v2, v207
	v_cvt_pk_fp8_f32 v2, v1, v3
	v_med3_f32 v1, v10, s74, v250
	v_med3_f32 v6, v11, s74, v250
	v_mov_b32_e32 v3, v207
	v_cvt_pk_fp8_f32 v3, v1, v6
	v_med3_f32 v4, v4, s74, v250
	v_med3_f32 v5, v5, s74, v250
	v_cvt_pk_fp8_f32 v2, v4, v5 op_sel:[0,0,1]
	v_med3_f32 v1, v8, s74, v250
	v_med3_f32 v4, v9, s74, v250
	v_cvt_pk_fp8_f32 v3, v1, v4 op_sel:[0,0,1]
	v_med3_f32 v1, v14, s74, v250
	v_med3_f32 v5, v15, s74, v250
	v_mov_b32_e32 v4, v207
	v_cvt_pk_fp8_f32 v4, v1, v5
	v_med3_f32 v1, v18, s74, v250
	v_med3_f32 v8, v19, s74, v250
	v_mov_b32_e32 v5, v207
	v_cvt_pk_fp8_f32 v5, v1, v8
	v_med3_f32 v6, v12, s74, v250
	v_med3_f32 v7, v13, s74, v250
	v_cvt_pk_fp8_f32 v4, v6, v7 op_sel:[0,0,1]
	v_med3_f32 v1, v16, s74, v250
	v_med3_f32 v6, v17, s74, v250
	v_cvt_pk_fp8_f32 v5, v1, v6 op_sel:[0,0,1]
	v_add_u32_e32 v0, 0xb0, v0
	v_ashrrev_i32_e32 v1, 31, v0
	v_lshlrev_b64 v[0:1], 11, v[0:1]
	ds_write_b128 v251, v[2:5] offset:1024
	ds_read_b128 v[2:5], v252 offset:1024
	v_lshl_add_u64 v[0:1], s[16:17], 0, v[0:1]
	v_lshl_add_u64 v[0:1], v[0:1], 0, s[40:41]
	v_lshl_add_u64 v[0:1], v[0:1], 0, s[12:13]
	v_lshl_add_u64 v[0:1], v[0:1], 0, v[214:215]
	s_and_b64 vcc, exec, s[0:1]
	s_mov_b64 s[0:1], -1
	s_waitcnt lgkmcnt(0)
	global_store_dwordx4 v[0:1], v[2:5], off nt
	s_cbranch_vccnz .LBB0_1942
	s_andn2_b64 vcc, exec, s[14:15]
	s_cbranch_vccnz .LBB0_1941
	s_barrier
	s_branch .LBB0_1941
